# GEMM K-loops: pointer bumps and trip test moved in front of the loop-back barrier (7 loops)
# speedup vs baseline: 1.0119x; 1.0042x over previous
.LBB0_447:
	ds_read_b128 v[132:135], v162
	ds_read_b128 v[136:139], v162 offset:1024
	ds_read_b128 v[140:143], v162 offset:2048
	ds_read_b128 v[144:147], v162 offset:3072
	ds_read_b128 v[148:151], v163
	ds_read_b128 v[152:155], v163 offset:1024
	ds_read_b128 v[168:171], v163 offset:2048
	ds_read_b128 v[172:175], v163 offset:3072
	s_add_i32 s28, s2, 2
	s_cmp_eq_u32 vcc_hi, s2
	s_cselect_b32 s60, s64, s24
	s_cselect_b32 s61, s23, s25
	s_cselect_b32 s58, vcc_lo, s26
	s_cselect_b32 s59, s65, s27
	s_add_u32 s2, s60, 0x80
	s_addc_u32 s3, s61, 0
	ds_read_b128 v[176:179], v164
	ds_read_b128 v[180:183], v164 offset:1024
	ds_read_b128 v[184:187], v164 offset:2048
	ds_read_b128 v[188:191], v164 offset:3072
	ds_read_b128 v[192:195], v164 offset:4096
	ds_read_b128 v[196:199], v164 offset:5120
	ds_read_b128 v[202:205], v164 offset:6144
	ds_read_b128 v[206:209], v164 offset:7168
	s_add_u32 s30, s24, 0x3ff80
	s_addc_u32 s31, s25, 0
	s_mov_b32 s29, m0
	s_mov_b32 m0, s78
	s_nop 0
	global_load_lds_dwordx4 v201, s[30:31]
	s_mov_b32 m0, s29
	s_nop 0
	s_mov_b32 s29, m0
	s_mov_b32 m0, s72
	s_nop 0
	global_load_lds_dwordx4 v160, s[30:31]
	s_mov_b32 m0, s29
	s_waitcnt vmcnt(8)
	s_waitcnt lgkmcnt(0)
	s_barrier
	s_setprio 1
	s_waitcnt lgkmcnt(6)
	v_mfma_scale_f32_16x16x128_f8f6f4 v[128:131], v[132:139], v[176:183], v[128:131], v165, v165 op_sel_hi:[0,0,0]
	v_mfma_scale_f32_16x16x128_f8f6f4 v[124:127], v[140:147], v[176:183], v[124:127], v165, v165 op_sel_hi:[0,0,0]
	s_waitcnt lgkmcnt(4)
	v_mfma_scale_f32_16x16x128_f8f6f4 v[112:115], v[132:139], v[184:191], v[112:115], v165, v165 op_sel_hi:[0,0,0]
	v_mfma_scale_f32_16x16x128_f8f6f4 v[108:111], v[140:147], v[184:191], v[108:111], v165, v165 op_sel_hi:[0,0,0]
	s_waitcnt lgkmcnt(2)
	v_mfma_scale_f32_16x16x128_f8f6f4 v[210:213], v[132:139], v[192:199], v[96:99], v165, v165 op_sel_hi:[0,0,0]
	v_mfma_scale_f32_16x16x128_f8f6f4 v[214:217], v[140:147], v[192:199], v[92:95], v165, v165 op_sel_hi:[0,0,0]
	s_waitcnt lgkmcnt(0)
	v_mfma_scale_f32_16x16x128_f8f6f4 v[218:221], v[132:139], v[202:209], v[80:83], v165, v165 op_sel_hi:[0,0,0]
	v_mfma_scale_f32_16x16x128_f8f6f4 v[222:225], v[140:147], v[202:209], v[76:79], v165, v165 op_sel_hi:[0,0,0]
	s_setprio 0
	s_setprio 1
	v_mfma_scale_f32_16x16x128_f8f6f4 v[120:123], v[148:155], v[176:183], v[120:123], v165, v165 op_sel_hi:[0,0,0]
	v_mfma_scale_f32_16x16x128_f8f6f4 v[116:119], v[168:175], v[176:183], v[116:119], v165, v165 op_sel_hi:[0,0,0]
	v_mfma_scale_f32_16x16x128_f8f6f4 v[104:107], v[148:155], v[184:191], v[104:107], v165, v165 op_sel_hi:[0,0,0]
	v_mfma_scale_f32_16x16x128_f8f6f4 v[100:103], v[168:175], v[184:191], v[100:103], v165, v165 op_sel_hi:[0,0,0]
	v_mfma_scale_f32_16x16x128_f8f6f4 v[176:179], v[148:155], v[192:199], v[88:91], v165, v165 op_sel_hi:[0,0,0]
	v_mfma_scale_f32_16x16x128_f8f6f4 v[180:183], v[168:175], v[192:199], v[84:87], v165, v165 op_sel_hi:[0,0,0]
	v_mfma_scale_f32_16x16x128_f8f6f4 v[184:187], v[148:155], v[202:209], v[72:75], v165, v165 op_sel_hi:[0,0,0]
	v_mfma_scale_f32_16x16x128_f8f6f4 v[188:191], v[168:175], v[202:209], v[68:71], v165, v165 op_sel_hi:[0,0,0]
	s_setprio 0
	s_barrier
	s_nop 4
	ds_read_b128 v[68:71], v164 offset:16384
	ds_read_b128 v[72:75], v164 offset:17408
	ds_read_b128 v[76:79], v164 offset:18432
	ds_read_b128 v[80:83], v164 offset:19456
	ds_read_b128 v[84:87], v164 offset:20480
	ds_read_b128 v[88:91], v164 offset:21504
	ds_read_b128 v[92:95], v164 offset:22528
	ds_read_b128 v[96:99], v164 offset:23552
	s_mov_b32 s29, m0
	s_mov_b32 m0, s84
	s_nop 0
	global_load_lds_dwordx4 v200, s[58:59]
	s_mov_b32 m0, s29
	s_add_u32 s30, s58, 0x40000
	s_mov_b32 s29, m0
	s_mov_b32 m0, s85
	s_nop 0
	global_load_lds_dwordx4 v161, s[58:59]
	s_mov_b32 m0, s29
	s_addc_u32 s31, s59, 0
	s_mov_b32 s29, m0
	s_mov_b32 m0, s86
	s_nop 0
	global_load_lds_dwordx4 v200, s[30:31]
	s_mov_b32 m0, s29
	s_nop 0
	s_mov_b32 s29, m0
	s_mov_b32 m0, s87
	s_nop 0
	global_load_lds_dwordx4 v161, s[30:31]
	s_mov_b32 m0, s29
	s_nop 0
	s_mov_b32 s29, m0
	s_mov_b32 m0, s83
	s_nop 0
	global_load_lds_dwordx4 v201, s[60:61]
	s_mov_b32 m0, s29
	s_nop 0
	s_mov_b32 s29, m0
	s_mov_b32 m0, s88
	s_nop 0
	global_load_lds_dwordx4 v160, s[60:61]
	s_mov_b32 m0, s29
	s_waitcnt vmcnt(8)
	s_waitcnt lgkmcnt(0)
	s_barrier
	s_setprio 1
	s_waitcnt lgkmcnt(6)
	v_mfma_scale_f32_16x16x128_f8f6f4 v[64:67], v[132:139], v[68:75], v[64:67], v165, v165 op_sel_hi:[0,0,0]
	v_mfma_scale_f32_16x16x128_f8f6f4 v[60:63], v[140:147], v[68:75], v[60:63], v165, v165 op_sel_hi:[0,0,0]
	s_waitcnt lgkmcnt(4)
	v_mfma_scale_f32_16x16x128_f8f6f4 v[192:195], v[132:139], v[76:83], v[48:51], v165, v165 op_sel_hi:[0,0,0]
	v_mfma_scale_f32_16x16x128_f8f6f4 v[196:199], v[140:147], v[76:83], v[44:47], v165, v165 op_sel_hi:[0,0,0]
	s_waitcnt lgkmcnt(2)
	v_mfma_scale_f32_16x16x128_f8f6f4 v[202:205], v[132:139], v[84:91], v[32:35], v165, v165 op_sel_hi:[0,0,0]
	v_mfma_scale_f32_16x16x128_f8f6f4 v[206:209], v[140:147], v[84:91], v[28:31], v165, v165 op_sel_hi:[0,0,0]
	s_waitcnt lgkmcnt(0)
	v_mfma_scale_f32_16x16x128_f8f6f4 v[226:229], v[132:139], v[92:99], v[16:19], v165, v165 op_sel_hi:[0,0,0]
	v_mfma_scale_f32_16x16x128_f8f6f4 v[230:233], v[140:147], v[92:99], v[12:15], v165, v165 op_sel_hi:[0,0,0]
	s_setprio 0
	s_setprio 1
	v_mfma_scale_f32_16x16x128_f8f6f4 v[56:59], v[148:155], v[68:75], v[56:59], v165, v165 op_sel_hi:[0,0,0]
	v_mfma_scale_f32_16x16x128_f8f6f4 v[52:55], v[168:175], v[68:75], v[52:55], v165, v165 op_sel_hi:[0,0,0]
	v_mfma_scale_f32_16x16x128_f8f6f4 v[234:237], v[148:155], v[76:83], v[40:43], v165, v165 op_sel_hi:[0,0,0]
	v_mfma_scale_f32_16x16x128_f8f6f4 v[238:241], v[168:175], v[76:83], v[36:39], v165, v165 op_sel_hi:[0,0,0]
	v_mfma_scale_f32_16x16x128_f8f6f4 v[242:245], v[148:155], v[84:91], v[24:27], v165, v165 op_sel_hi:[0,0,0]
	v_mfma_scale_f32_16x16x128_f8f6f4 v[246:249], v[168:175], v[84:91], v[20:23], v165, v165 op_sel_hi:[0,0,0]
	v_mfma_scale_f32_16x16x128_f8f6f4 v[250:253], v[148:155], v[92:99], v[8:11], v165, v165 op_sel_hi:[0,0,0]
	v_mfma_scale_f32_16x16x128_f8f6f4 v[156:159], v[168:175], v[92:99], v[4:7], v165, v165 op_sel_hi:[0,0,0]
	s_setprio 0
	s_barrier
	s_nop 4
	ds_read_b128 v[4:7], v166
	ds_read_b128 v[8:11], v166 offset:1024
	ds_read_b128 v[20:23], v166 offset:2048
	ds_read_b128 v[24:27], v166 offset:3072
	ds_read_b128 v[132:135], v167
	ds_read_b128 v[136:139], v167 offset:1024
	ds_read_b128 v[140:143], v167 offset:2048
	ds_read_b128 v[144:147], v167 offset:3072
	ds_read_b128 v[12:15], v164 offset:32768
	ds_read_b128 v[16:19], v164 offset:33792
	ds_read_b128 v[28:31], v164 offset:34816
	ds_read_b128 v[32:35], v164 offset:35840
	ds_read_b128 v[36:39], v164 offset:36864
	ds_read_b128 v[40:43], v164 offset:37888
	ds_read_b128 v[44:47], v164 offset:38912
	ds_read_b128 v[48:51], v164 offset:39936
	s_add_u32 s30, s60, 0x40000
	s_addc_u32 s31, s61, 0
	s_mov_b32 s29, m0
	s_mov_b32 m0, s89
	s_nop 0
	global_load_lds_dwordx4 v201, s[30:31]
	s_mov_b32 m0, s29
	s_nop 0
	s_mov_b32 s29, m0
	s_mov_b32 m0, s90
	s_nop 0
	global_load_lds_dwordx4 v160, s[30:31]
	s_mov_b32 m0, s29
	s_waitcnt vmcnt(8)
	s_waitcnt lgkmcnt(0)
	s_barrier
	s_setprio 1
	s_waitcnt lgkmcnt(6)
	v_mfma_scale_f32_16x16x128_f8f6f4 v[128:131], v[4:11], v[12:19], v[128:131], v165, v165 op_sel_hi:[0,0,0]
	v_mfma_scale_f32_16x16x128_f8f6f4 v[124:127], v[20:27], v[12:19], v[124:127], v165, v165 op_sel_hi:[0,0,0]
	s_waitcnt lgkmcnt(4)
	v_mfma_scale_f32_16x16x128_f8f6f4 v[112:115], v[4:11], v[28:35], v[112:115], v165, v165 op_sel_hi:[0,0,0]
	v_mfma_scale_f32_16x16x128_f8f6f4 v[108:111], v[20:27], v[28:35], v[108:111], v165, v165 op_sel_hi:[0,0,0]
	s_waitcnt lgkmcnt(2)
	v_mfma_scale_f32_16x16x128_f8f6f4 v[96:99], v[4:11], v[36:43], v[210:213], v165, v165 op_sel_hi:[0,0,0]
	v_mfma_scale_f32_16x16x128_f8f6f4 v[92:95], v[20:27], v[36:43], v[214:217], v165, v165 op_sel_hi:[0,0,0]
	s_waitcnt lgkmcnt(0)
	v_mfma_scale_f32_16x16x128_f8f6f4 v[80:83], v[4:11], v[44:51], v[218:221], v165, v165 op_sel_hi:[0,0,0]
	v_mfma_scale_f32_16x16x128_f8f6f4 v[76:79], v[20:27], v[44:51], v[222:225], v165, v165 op_sel_hi:[0,0,0]
	s_setprio 0
	s_setprio 1
	v_mfma_scale_f32_16x16x128_f8f6f4 v[120:123], v[132:139], v[12:19], v[120:123], v165, v165 op_sel_hi:[0,0,0]
	v_mfma_scale_f32_16x16x128_f8f6f4 v[116:119], v[140:147], v[12:19], v[116:119], v165, v165 op_sel_hi:[0,0,0]
	v_mfma_scale_f32_16x16x128_f8f6f4 v[104:107], v[132:139], v[28:35], v[104:107], v165, v165 op_sel_hi:[0,0,0]
	v_mfma_scale_f32_16x16x128_f8f6f4 v[100:103], v[140:147], v[28:35], v[100:103], v165, v165 op_sel_hi:[0,0,0]
	v_mfma_scale_f32_16x16x128_f8f6f4 v[88:91], v[132:139], v[36:43], v[176:179], v165, v165 op_sel_hi:[0,0,0]
	v_mfma_scale_f32_16x16x128_f8f6f4 v[84:87], v[140:147], v[36:43], v[180:183], v165, v165 op_sel_hi:[0,0,0]
	v_mfma_scale_f32_16x16x128_f8f6f4 v[72:75], v[132:139], v[44:51], v[184:187], v165, v165 op_sel_hi:[0,0,0]
	v_mfma_scale_f32_16x16x128_f8f6f4 v[68:71], v[140:147], v[44:51], v[188:191], v165, v165 op_sel_hi:[0,0,0]
	s_setprio 0
	s_barrier
	ds_read_b128 v[36:39], v164 offset:49152
	ds_read_b128 v[40:43], v164 offset:50176
	ds_read_b128 v[148:151], v164 offset:51200
	ds_read_b128 v[152:155], v164 offset:52224
	ds_read_b128 v[168:171], v164 offset:53248
	ds_read_b128 v[172:175], v164 offset:54272
	ds_read_b128 v[176:179], v164 offset:55296
	ds_read_b128 v[180:183], v164 offset:56320
	s_add_u32 s30, s58, 0x80
	s_addc_u32 s31, s59, 0
	s_mov_b32 s29, m0
	s_mov_b32 m0, s93
	s_nop 0
	global_load_lds_dwordx4 v200, s[30:31]
	s_mov_b32 m0, s29
	s_nop 0
	s_mov_b32 s29, m0
	s_mov_b32 m0, s94
	s_nop 0
	global_load_lds_dwordx4 v161, s[30:31]
	s_mov_b32 m0, s29
	s_add_u32 s30, s58, 0x40080
	s_addc_u32 s31, s59, 0
	s_mov_b32 s29, m0
	s_mov_b32 m0, s97
	s_nop 0
	global_load_lds_dwordx4 v200, s[30:31]
	s_mov_b32 m0, s29
	s_nop 0
	s_mov_b32 s29, m0
	s_mov_b32 m0, s80
	s_nop 0
	global_load_lds_dwordx4 v161, s[30:31]
	s_mov_b32 m0, s29
	s_nop 0
	s_mov_b32 s29, m0
	s_mov_b32 m0, s95
	s_nop 0
	global_load_lds_dwordx4 v201, s[2:3]
	s_mov_b32 m0, s29
	s_nop 0
	s_mov_b32 s29, m0
	s_mov_b32 m0, s96
	s_nop 0
	global_load_lds_dwordx4 v160, s[2:3]
	s_mov_b32 m0, s29
	s_waitcnt vmcnt(8)
	s_waitcnt lgkmcnt(0)
	s_barrier
	s_setprio 1
	s_waitcnt lgkmcnt(6)
	v_mfma_scale_f32_16x16x128_f8f6f4 v[64:67], v[4:11], v[36:43], v[64:67], v165, v165 op_sel_hi:[0,0,0]
	v_mfma_scale_f32_16x16x128_f8f6f4 v[60:63], v[20:27], v[36:43], v[60:63], v165, v165 op_sel_hi:[0,0,0]
	s_waitcnt lgkmcnt(4)
	v_mfma_scale_f32_16x16x128_f8f6f4 v[48:51], v[4:11], v[148:155], v[192:195], v165, v165 op_sel_hi:[0,0,0]
	v_mfma_scale_f32_16x16x128_f8f6f4 v[44:47], v[20:27], v[148:155], v[196:199], v165, v165 op_sel_hi:[0,0,0]
	s_waitcnt lgkmcnt(2)
	v_mfma_scale_f32_16x16x128_f8f6f4 v[32:35], v[4:11], v[168:175], v[202:205], v165, v165 op_sel_hi:[0,0,0]
	v_mfma_scale_f32_16x16x128_f8f6f4 v[28:31], v[20:27], v[168:175], v[206:209], v165, v165 op_sel_hi:[0,0,0]
	s_waitcnt lgkmcnt(0)
	v_mfma_scale_f32_16x16x128_f8f6f4 v[16:19], v[4:11], v[176:183], v[226:229], v165, v165 op_sel_hi:[0,0,0]
	v_mfma_scale_f32_16x16x128_f8f6f4 v[12:15], v[20:27], v[176:183], v[230:233], v165, v165 op_sel_hi:[0,0,0]
	s_setprio 0
	s_setprio 1
	v_mfma_scale_f32_16x16x128_f8f6f4 v[56:59], v[132:139], v[36:43], v[56:59], v165, v165 op_sel_hi:[0,0,0]
	v_mfma_scale_f32_16x16x128_f8f6f4 v[52:55], v[140:147], v[36:43], v[52:55], v165, v165 op_sel_hi:[0,0,0]
	v_mfma_scale_f32_16x16x128_f8f6f4 v[40:43], v[132:139], v[148:155], v[234:237], v165, v165 op_sel_hi:[0,0,0]
	v_mfma_scale_f32_16x16x128_f8f6f4 v[36:39], v[140:147], v[148:155], v[238:241], v165, v165 op_sel_hi:[0,0,0]
	v_mfma_scale_f32_16x16x128_f8f6f4 v[24:27], v[132:139], v[168:175], v[242:245], v165, v165 op_sel_hi:[0,0,0]
	v_mfma_scale_f32_16x16x128_f8f6f4 v[20:23], v[140:147], v[168:175], v[246:249], v165, v165 op_sel_hi:[0,0,0]
	v_mfma_scale_f32_16x16x128_f8f6f4 v[8:11], v[132:139], v[176:183], v[250:253], v165, v165 op_sel_hi:[0,0,0]
	v_mfma_scale_f32_16x16x128_f8f6f4 v[4:7], v[140:147], v[176:183], v[156:159], v165, v165 op_sel_hi:[0,0,0]
	s_add_u32 s24, s24, 0x100
	s_addc_u32 s25, s25, 0
	s_add_u32 s26, s26, 0x100
	s_addc_u32 s27, s27, 0
	s_cmp_ge_i32 s28, s14
	s_mov_b32 s2, s28
	s_setprio 0
	s_barrier
	s_cbranch_scc0 .LBB0_447
	s_and_b64 vcc, exec, s[20:21]
	s_cbranch_vccz .LBB0_450

.LBB0_762:
	ds_read_b128 v[132:135], v148
	ds_read_b128 v[136:139], v148 offset:1024
	ds_read_b128 v[154:157], v148 offset:2048
	ds_read_b128 v[158:161], v148 offset:3072
	ds_read_b128 v[162:165], v149
	ds_read_b128 v[166:169], v149 offset:1024
	ds_read_b128 v[170:173], v149 offset:2048
	ds_read_b128 v[174:177], v149 offset:3072
	s_add_i32 s91, s30, 2
	s_cmp_eq_u32 s86, s30
	s_cselect_b32 s42, s45, s87
	s_cselect_b32 s43, s44, s88
	s_cselect_b32 s34, s85, s89
	s_cselect_b32 s35, s84, s90
	s_add_u32 s30, s42, 0x80
	s_addc_u32 s31, s43, 0
	ds_read_b128 v[178:181], v150
	ds_read_b128 v[182:185], v150 offset:1024
	ds_read_b128 v[186:189], v150 offset:2048
	ds_read_b128 v[190:193], v150 offset:3072
	ds_read_b128 v[202:205], v150 offset:4096
	ds_read_b128 v[206:209], v150 offset:5120
	ds_read_b128 v[210:213], v150 offset:6144
	ds_read_b128 v[214:217], v150 offset:7168
	s_add_u32 s92, s87, 0x3ff80
	s_addc_u32 s93, s88, 0
	s_mov_b32 s94, m0
	s_mov_b32 m0, s72
	s_nop 0
	global_load_lds_dwordx4 v144, s[92:93]
	s_mov_b32 m0, s94
	s_nop 0
	s_mov_b32 s94, m0
	s_mov_b32 m0, s73
	s_nop 0
	global_load_lds_dwordx4 v146, s[92:93]
	s_mov_b32 m0, s94
	s_waitcnt vmcnt(8)
	s_waitcnt lgkmcnt(0)
	s_barrier
	s_setprio 1
	s_waitcnt lgkmcnt(6)
	v_mfma_scale_f32_16x16x128_f8f6f4 v[128:131], v[132:139], v[178:185], v[128:131], v151, v151 op_sel_hi:[0,0,0]
	v_mfma_scale_f32_16x16x128_f8f6f4 v[124:127], v[154:161], v[178:185], v[124:127], v151, v151 op_sel_hi:[0,0,0]
	s_waitcnt lgkmcnt(4)
	v_mfma_scale_f32_16x16x128_f8f6f4 v[112:115], v[132:139], v[186:193], v[112:115], v151, v151 op_sel_hi:[0,0,0]
	v_mfma_scale_f32_16x16x128_f8f6f4 v[108:111], v[154:161], v[186:193], v[108:111], v151, v151 op_sel_hi:[0,0,0]
	s_waitcnt lgkmcnt(2)
	v_mfma_scale_f32_16x16x128_f8f6f4 v[140:143], v[132:139], v[202:209], v[96:99], v151, v151 op_sel_hi:[0,0,0]
	v_mfma_scale_f32_16x16x128_f8f6f4 v[194:197], v[154:161], v[202:209], v[92:95], v151, v151 op_sel_hi:[0,0,0]
	s_waitcnt lgkmcnt(0)
	v_mfma_scale_f32_16x16x128_f8f6f4 v[218:221], v[132:139], v[210:217], v[80:83], v151, v151 op_sel_hi:[0,0,0]
	v_mfma_scale_f32_16x16x128_f8f6f4 v[222:225], v[154:161], v[210:217], v[76:79], v151, v151 op_sel_hi:[0,0,0]
	s_setprio 0
	s_setprio 1
	v_mfma_scale_f32_16x16x128_f8f6f4 v[120:123], v[162:169], v[178:185], v[120:123], v151, v151 op_sel_hi:[0,0,0]
	v_mfma_scale_f32_16x16x128_f8f6f4 v[116:119], v[170:177], v[178:185], v[116:119], v151, v151 op_sel_hi:[0,0,0]
	v_mfma_scale_f32_16x16x128_f8f6f4 v[104:107], v[162:169], v[186:193], v[104:107], v151, v151 op_sel_hi:[0,0,0]
	v_mfma_scale_f32_16x16x128_f8f6f4 v[100:103], v[170:177], v[186:193], v[100:103], v151, v151 op_sel_hi:[0,0,0]
	v_mfma_scale_f32_16x16x128_f8f6f4 v[178:181], v[162:169], v[202:209], v[88:91], v151, v151 op_sel_hi:[0,0,0]
	v_mfma_scale_f32_16x16x128_f8f6f4 v[182:185], v[170:177], v[202:209], v[84:87], v151, v151 op_sel_hi:[0,0,0]
	v_mfma_scale_f32_16x16x128_f8f6f4 v[186:189], v[162:169], v[210:217], v[72:75], v151, v151 op_sel_hi:[0,0,0]
	v_mfma_scale_f32_16x16x128_f8f6f4 v[190:193], v[170:177], v[210:217], v[68:71], v151, v151 op_sel_hi:[0,0,0]
	s_setprio 0
	s_barrier
	s_nop 4
	ds_read_b128 v[68:71], v150 offset:16384
	ds_read_b128 v[72:75], v150 offset:17408
	ds_read_b128 v[76:79], v150 offset:18432
	ds_read_b128 v[80:83], v150 offset:19456
	ds_read_b128 v[84:87], v150 offset:20480
	ds_read_b128 v[88:91], v150 offset:21504
	ds_read_b128 v[92:95], v150 offset:22528
	ds_read_b128 v[96:99], v150 offset:23552
	s_mov_b32 s92, m0
	s_mov_b32 m0, s46
	s_nop 0
	global_load_lds_dwordx4 v145, s[34:35]
	s_mov_b32 m0, s92
	s_nop 0
	s_mov_b32 s92, m0
	s_mov_b32 m0, s47
	s_nop 0
	global_load_lds_dwordx4 v147, s[34:35]
	s_mov_b32 m0, s92
	s_add_u32 s92, s34, 0x40000
	s_addc_u32 s93, s35, 0
	s_mov_b32 s94, m0
	s_mov_b32 m0, s52
	s_nop 0
	global_load_lds_dwordx4 v145, s[92:93]
	s_mov_b32 m0, s94
	s_nop 0
	s_mov_b32 s94, m0
	s_mov_b32 m0, s53
	s_nop 0
	global_load_lds_dwordx4 v147, s[92:93]
	s_mov_b32 m0, s94
	s_mov_b32 s92, m0
	s_mov_b32 m0, s17
	s_nop 0
	global_load_lds_dwordx4 v144, s[42:43]
	s_mov_b32 m0, s92
	s_nop 0
	s_mov_b32 s92, m0
	s_mov_b32 m0, s55
	s_nop 0
	global_load_lds_dwordx4 v146, s[42:43]
	s_mov_b32 m0, s92
	s_waitcnt vmcnt(8)
	s_waitcnt lgkmcnt(0)
	s_barrier
	s_setprio 1
	s_waitcnt lgkmcnt(6)
	v_mfma_scale_f32_16x16x128_f8f6f4 v[64:67], v[132:139], v[68:75], v[64:67], v151, v151 op_sel_hi:[0,0,0]
	v_mfma_scale_f32_16x16x128_f8f6f4 v[60:63], v[154:161], v[68:75], v[60:63], v151, v151 op_sel_hi:[0,0,0]
	s_waitcnt lgkmcnt(4)
	v_mfma_scale_f32_16x16x128_f8f6f4 v[202:205], v[132:139], v[76:83], v[48:51], v151, v151 op_sel_hi:[0,0,0]
	v_mfma_scale_f32_16x16x128_f8f6f4 v[206:209], v[154:161], v[76:83], v[44:47], v151, v151 op_sel_hi:[0,0,0]
	s_waitcnt lgkmcnt(2)
	v_mfma_scale_f32_16x16x128_f8f6f4 v[210:213], v[132:139], v[84:91], v[32:35], v151, v151 op_sel_hi:[0,0,0]
	v_mfma_scale_f32_16x16x128_f8f6f4 v[214:217], v[154:161], v[84:91], v[28:31], v151, v151 op_sel_hi:[0,0,0]
	s_waitcnt lgkmcnt(0)
	v_mfma_scale_f32_16x16x128_f8f6f4 v[226:229], v[132:139], v[92:99], v[16:19], v151, v151 op_sel_hi:[0,0,0]
	v_mfma_scale_f32_16x16x128_f8f6f4 v[230:233], v[154:161], v[92:99], v[12:15], v151, v151 op_sel_hi:[0,0,0]
	s_setprio 0
	s_setprio 1
	v_mfma_scale_f32_16x16x128_f8f6f4 v[56:59], v[162:169], v[68:75], v[56:59], v151, v151 op_sel_hi:[0,0,0]
	v_mfma_scale_f32_16x16x128_f8f6f4 v[52:55], v[170:177], v[68:75], v[52:55], v151, v151 op_sel_hi:[0,0,0]
	v_mfma_scale_f32_16x16x128_f8f6f4 v[234:237], v[162:169], v[76:83], v[40:43], v151, v151 op_sel_hi:[0,0,0]
	v_mfma_scale_f32_16x16x128_f8f6f4 v[238:241], v[170:177], v[76:83], v[36:39], v151, v151 op_sel_hi:[0,0,0]
	v_mfma_scale_f32_16x16x128_f8f6f4 v[242:245], v[162:169], v[84:91], v[24:27], v151, v151 op_sel_hi:[0,0,0]
	v_mfma_scale_f32_16x16x128_f8f6f4 v[246:249], v[170:177], v[84:91], v[20:23], v151, v151 op_sel_hi:[0,0,0]
	v_mfma_scale_f32_16x16x128_f8f6f4 v[250:253], v[162:169], v[92:99], v[8:11], v151, v151 op_sel_hi:[0,0,0]
	v_mfma_scale_f32_16x16x128_f8f6f4 v[198:201], v[170:177], v[92:99], v[4:7], v151, v151 op_sel_hi:[0,0,0]
	s_setprio 0
	s_barrier
	s_nop 4
	ds_read_b128 v[4:7], v152
	ds_read_b128 v[8:11], v152 offset:1024
	ds_read_b128 v[20:23], v152 offset:2048
	ds_read_b128 v[24:27], v152 offset:3072
	ds_read_b128 v[132:135], v153
	ds_read_b128 v[136:139], v153 offset:1024
	ds_read_b128 v[154:157], v153 offset:2048
	ds_read_b128 v[158:161], v153 offset:3072
	ds_read_b128 v[12:15], v150 offset:32768
	ds_read_b128 v[16:19], v150 offset:33792
	ds_read_b128 v[28:31], v150 offset:34816
	ds_read_b128 v[32:35], v150 offset:35840
	ds_read_b128 v[36:39], v150 offset:36864
	ds_read_b128 v[40:43], v150 offset:37888
	ds_read_b128 v[44:47], v150 offset:38912
	ds_read_b128 v[48:51], v150 offset:39936
	s_add_u32 s42, s42, 0x40000
	s_addc_u32 s43, s43, 0
	s_mov_b32 s92, m0
	s_mov_b32 m0, s56
	s_nop 0
	global_load_lds_dwordx4 v144, s[42:43]
	s_mov_b32 m0, s92
	s_nop 0
	s_mov_b32 s92, m0
	s_mov_b32 m0, s57
	s_nop 0
	global_load_lds_dwordx4 v146, s[42:43]
	s_mov_b32 m0, s92
	s_waitcnt vmcnt(8)
	s_waitcnt lgkmcnt(0)
	s_barrier
	s_setprio 1
	s_waitcnt lgkmcnt(6)
	v_mfma_scale_f32_16x16x128_f8f6f4 v[128:131], v[4:11], v[12:19], v[128:131], v151, v151 op_sel_hi:[0,0,0]
	v_mfma_scale_f32_16x16x128_f8f6f4 v[124:127], v[20:27], v[12:19], v[124:127], v151, v151 op_sel_hi:[0,0,0]
	s_waitcnt lgkmcnt(4)
	v_mfma_scale_f32_16x16x128_f8f6f4 v[112:115], v[4:11], v[28:35], v[112:115], v151, v151 op_sel_hi:[0,0,0]
	v_mfma_scale_f32_16x16x128_f8f6f4 v[108:111], v[20:27], v[28:35], v[108:111], v151, v151 op_sel_hi:[0,0,0]
	s_waitcnt lgkmcnt(2)
	v_mfma_scale_f32_16x16x128_f8f6f4 v[96:99], v[4:11], v[36:43], v[140:143], v151, v151 op_sel_hi:[0,0,0]
	v_mfma_scale_f32_16x16x128_f8f6f4 v[92:95], v[20:27], v[36:43], v[194:197], v151, v151 op_sel_hi:[0,0,0]
	s_waitcnt lgkmcnt(0)
	v_mfma_scale_f32_16x16x128_f8f6f4 v[80:83], v[4:11], v[44:51], v[218:221], v151, v151 op_sel_hi:[0,0,0]
	v_mfma_scale_f32_16x16x128_f8f6f4 v[76:79], v[20:27], v[44:51], v[222:225], v151, v151 op_sel_hi:[0,0,0]
	s_setprio 0
	s_setprio 1
	v_mfma_scale_f32_16x16x128_f8f6f4 v[120:123], v[132:139], v[12:19], v[120:123], v151, v151 op_sel_hi:[0,0,0]
	v_mfma_scale_f32_16x16x128_f8f6f4 v[116:119], v[154:161], v[12:19], v[116:119], v151, v151 op_sel_hi:[0,0,0]
	v_mfma_scale_f32_16x16x128_f8f6f4 v[104:107], v[132:139], v[28:35], v[104:107], v151, v151 op_sel_hi:[0,0,0]
	v_mfma_scale_f32_16x16x128_f8f6f4 v[100:103], v[154:161], v[28:35], v[100:103], v151, v151 op_sel_hi:[0,0,0]
	v_mfma_scale_f32_16x16x128_f8f6f4 v[88:91], v[132:139], v[36:43], v[178:181], v151, v151 op_sel_hi:[0,0,0]
	v_mfma_scale_f32_16x16x128_f8f6f4 v[84:87], v[154:161], v[36:43], v[182:185], v151, v151 op_sel_hi:[0,0,0]
	v_mfma_scale_f32_16x16x128_f8f6f4 v[72:75], v[132:139], v[44:51], v[186:189], v151, v151 op_sel_hi:[0,0,0]
	v_mfma_scale_f32_16x16x128_f8f6f4 v[68:71], v[154:161], v[44:51], v[190:193], v151, v151 op_sel_hi:[0,0,0]
	s_setprio 0
	s_barrier
	ds_read_b128 v[36:39], v150 offset:49152
	ds_read_b128 v[40:43], v150 offset:50176
	ds_read_b128 v[162:165], v150 offset:51200
	ds_read_b128 v[166:169], v150 offset:52224
	ds_read_b128 v[170:173], v150 offset:53248
	ds_read_b128 v[174:177], v150 offset:54272
	ds_read_b128 v[178:181], v150 offset:55296
	ds_read_b128 v[182:185], v150 offset:56320
	s_add_u32 s42, s34, 0x80
	s_addc_u32 s43, s35, 0
	s_mov_b32 s92, m0
	s_mov_b32 m0, s60
	s_nop 0
	global_load_lds_dwordx4 v145, s[42:43]
	s_mov_b32 m0, s92
	s_add_u32 s34, s34, 0x40080
	s_mov_b32 s92, m0
	s_mov_b32 m0, s61
	s_nop 0
	global_load_lds_dwordx4 v147, s[42:43]
	s_mov_b32 m0, s92
	s_addc_u32 s35, s35, 0
	s_mov_b32 s42, m0
	s_mov_b32 m0, s68
	s_nop 0
	global_load_lds_dwordx4 v145, s[34:35]
	s_mov_b32 m0, s42
	s_nop 0
	s_mov_b32 s42, m0
	s_mov_b32 m0, s69
	s_nop 0
	global_load_lds_dwordx4 v147, s[34:35]
	s_mov_b32 m0, s42
	s_mov_b32 s34, m0
	s_mov_b32 m0, s64
	s_nop 0
	global_load_lds_dwordx4 v144, s[30:31]
	s_mov_b32 m0, s34
	s_nop 0
	s_mov_b32 s34, m0
	s_mov_b32 m0, s65
	s_nop 0
	global_load_lds_dwordx4 v146, s[30:31]
	s_mov_b32 m0, s34
	s_waitcnt vmcnt(8)
	s_waitcnt lgkmcnt(0)
	s_barrier
	s_setprio 1
	s_waitcnt lgkmcnt(6)
	v_mfma_scale_f32_16x16x128_f8f6f4 v[64:67], v[4:11], v[36:43], v[64:67], v151, v151 op_sel_hi:[0,0,0]
	v_mfma_scale_f32_16x16x128_f8f6f4 v[60:63], v[20:27], v[36:43], v[60:63], v151, v151 op_sel_hi:[0,0,0]
	s_waitcnt lgkmcnt(4)
	v_mfma_scale_f32_16x16x128_f8f6f4 v[48:51], v[4:11], v[162:169], v[202:205], v151, v151 op_sel_hi:[0,0,0]
	v_mfma_scale_f32_16x16x128_f8f6f4 v[44:47], v[20:27], v[162:169], v[206:209], v151, v151 op_sel_hi:[0,0,0]
	s_waitcnt lgkmcnt(2)
	v_mfma_scale_f32_16x16x128_f8f6f4 v[32:35], v[4:11], v[170:177], v[210:213], v151, v151 op_sel_hi:[0,0,0]
	v_mfma_scale_f32_16x16x128_f8f6f4 v[28:31], v[20:27], v[170:177], v[214:217], v151, v151 op_sel_hi:[0,0,0]
	s_waitcnt lgkmcnt(0)
	v_mfma_scale_f32_16x16x128_f8f6f4 v[16:19], v[4:11], v[178:185], v[226:229], v151, v151 op_sel_hi:[0,0,0]
	v_mfma_scale_f32_16x16x128_f8f6f4 v[12:15], v[20:27], v[178:185], v[230:233], v151, v151 op_sel_hi:[0,0,0]
	s_setprio 0
	s_setprio 1
	v_mfma_scale_f32_16x16x128_f8f6f4 v[56:59], v[132:139], v[36:43], v[56:59], v151, v151 op_sel_hi:[0,0,0]
	v_mfma_scale_f32_16x16x128_f8f6f4 v[52:55], v[154:161], v[36:43], v[52:55], v151, v151 op_sel_hi:[0,0,0]
	v_mfma_scale_f32_16x16x128_f8f6f4 v[40:43], v[132:139], v[162:169], v[234:237], v151, v151 op_sel_hi:[0,0,0]
	v_mfma_scale_f32_16x16x128_f8f6f4 v[36:39], v[154:161], v[162:169], v[238:241], v151, v151 op_sel_hi:[0,0,0]
	v_mfma_scale_f32_16x16x128_f8f6f4 v[24:27], v[132:139], v[170:177], v[242:245], v151, v151 op_sel_hi:[0,0,0]
	v_mfma_scale_f32_16x16x128_f8f6f4 v[20:23], v[154:161], v[170:177], v[246:249], v151, v151 op_sel_hi:[0,0,0]
	v_mfma_scale_f32_16x16x128_f8f6f4 v[8:11], v[132:139], v[178:185], v[250:253], v151, v151 op_sel_hi:[0,0,0]
	v_mfma_scale_f32_16x16x128_f8f6f4 v[4:7], v[154:161], v[178:185], v[198:201], v151, v151 op_sel_hi:[0,0,0]
	s_add_u32 s87, s87, 0x100
	s_addc_u32 s88, s88, 0
	s_add_u32 s89, s89, 0x100
	s_addc_u32 s90, s90, 0
	s_cmp_ge_i32 s91, s27
	s_mov_b32 s30, s91
	s_setprio 0
	s_barrier
	s_cbranch_scc0 .LBB0_762
	s_and_b64 vcc, exec, s[10:11]
	s_cbranch_vccz .LBB0_765

.LBB0_1262:
	ds_read_b128 v[132:135], v150
	ds_read_b128 v[136:139], v150 offset:1024
	ds_read_b128 v[156:159], v150 offset:2048
	ds_read_b128 v[160:163], v150 offset:3072
	ds_read_b128 v[164:167], v151
	ds_read_b128 v[168:171], v151 offset:1024
	ds_read_b128 v[172:175], v151 offset:2048
	ds_read_b128 v[176:179], v151 offset:3072
	s_add_i32 s44, s30, 2
	s_cmp_eq_u32 s96, s30
	s_cselect_b32 s42, s93, s97
	s_cselect_b32 s43, s23, vcc_lo
	s_cselect_b32 s34, s95, vcc_hi
	s_cselect_b32 s35, s94, s53
	s_add_u32 s30, s42, 0x80
	s_addc_u32 s31, s43, 0
	ds_read_b128 v[180:183], v152
	ds_read_b128 v[184:187], v152 offset:1024
	ds_read_b128 v[202:205], v152 offset:2048
	ds_read_b128 v[206:209], v152 offset:3072
	ds_read_b128 v[210:213], v152 offset:4096
	ds_read_b128 v[214:217], v152 offset:5120
	ds_read_b128 v[218:221], v152 offset:6144
	ds_read_b128 v[222:225], v152 offset:7168
	s_add_u32 s46, s97, 0x3ff80
	s_addc_u32 s47, vcc_lo, 0
	s_mov_b32 s7, m0
	s_mov_b32 m0, s80
	s_nop 0
	global_load_lds_dwordx4 v1, s[46:47]
	s_mov_b32 m0, s7
	s_nop 0
	s_mov_b32 s7, m0
	s_mov_b32 m0, s81
	s_nop 0
	global_load_lds_dwordx4 v148, s[46:47]
	s_mov_b32 m0, s7
	s_waitcnt vmcnt(8)
	s_waitcnt lgkmcnt(0)
	s_barrier
	s_setprio 1
	s_waitcnt lgkmcnt(6)
	v_mfma_scale_f32_16x16x128_f8f6f4 v[128:131], v[132:139], v[180:187], v[128:131], v153, v153 op_sel_hi:[0,0,0]
	v_mfma_scale_f32_16x16x128_f8f6f4 v[124:127], v[156:163], v[180:187], v[124:127], v153, v153 op_sel_hi:[0,0,0]
	s_waitcnt lgkmcnt(4)
	v_mfma_scale_f32_16x16x128_f8f6f4 v[112:115], v[132:139], v[202:209], v[112:115], v153, v153 op_sel_hi:[0,0,0]
	v_mfma_scale_f32_16x16x128_f8f6f4 v[108:111], v[156:163], v[202:209], v[108:111], v153, v153 op_sel_hi:[0,0,0]
	s_waitcnt lgkmcnt(2)
	v_mfma_scale_f32_16x16x128_f8f6f4 v[140:143], v[132:139], v[210:217], v[96:99], v153, v153 op_sel_hi:[0,0,0]
	v_mfma_scale_f32_16x16x128_f8f6f4 v[188:191], v[156:163], v[210:217], v[92:95], v153, v153 op_sel_hi:[0,0,0]
	s_waitcnt lgkmcnt(0)
	v_mfma_scale_f32_16x16x128_f8f6f4 v[194:197], v[132:139], v[218:225], v[80:83], v153, v153 op_sel_hi:[0,0,0]
	v_mfma_scale_f32_16x16x128_f8f6f4 v[198:201], v[156:163], v[218:225], v[76:79], v153, v153 op_sel_hi:[0,0,0]
	s_setprio 0
	s_setprio 1
	v_mfma_scale_f32_16x16x128_f8f6f4 v[120:123], v[164:171], v[180:187], v[120:123], v153, v153 op_sel_hi:[0,0,0]
	v_mfma_scale_f32_16x16x128_f8f6f4 v[116:119], v[172:179], v[180:187], v[116:119], v153, v153 op_sel_hi:[0,0,0]
	v_mfma_scale_f32_16x16x128_f8f6f4 v[104:107], v[164:171], v[202:209], v[104:107], v153, v153 op_sel_hi:[0,0,0]
	v_mfma_scale_f32_16x16x128_f8f6f4 v[100:103], v[172:179], v[202:209], v[100:103], v153, v153 op_sel_hi:[0,0,0]
	v_mfma_scale_f32_16x16x128_f8f6f4 v[180:183], v[164:171], v[210:217], v[88:91], v153, v153 op_sel_hi:[0,0,0]
	v_mfma_scale_f32_16x16x128_f8f6f4 v[184:187], v[172:179], v[210:217], v[84:87], v153, v153 op_sel_hi:[0,0,0]
	v_mfma_scale_f32_16x16x128_f8f6f4 v[202:205], v[164:171], v[218:225], v[72:75], v153, v153 op_sel_hi:[0,0,0]
	v_mfma_scale_f32_16x16x128_f8f6f4 v[206:209], v[172:179], v[218:225], v[68:71], v153, v153 op_sel_hi:[0,0,0]
	s_setprio 0
	s_barrier
	s_nop 4
	ds_read_b128 v[68:71], v152 offset:16384
	ds_read_b128 v[72:75], v152 offset:17408
	ds_read_b128 v[76:79], v152 offset:18432
	ds_read_b128 v[80:83], v152 offset:19456
	ds_read_b128 v[84:87], v152 offset:20480
	ds_read_b128 v[88:91], v152 offset:21504
	ds_read_b128 v[92:95], v152 offset:22528
	ds_read_b128 v[96:99], v152 offset:23552
	s_mov_b32 s7, m0
	s_mov_b32 m0, s55
	s_nop 0
	global_load_lds_dwordx4 v193, s[34:35]
	s_mov_b32 m0, s7
	s_add_u32 s46, s34, 0x40000
	s_mov_b32 s7, m0
	s_mov_b32 m0, s57
	s_nop 0
	global_load_lds_dwordx4 v149, s[34:35]
	s_mov_b32 m0, s7
	s_addc_u32 s47, s35, 0
	s_mov_b32 s7, m0
	s_mov_b32 m0, s58
	s_nop 0
	global_load_lds_dwordx4 v193, s[46:47]
	s_mov_b32 m0, s7
	s_nop 0
	s_mov_b32 s7, m0
	s_mov_b32 m0, s59
	s_nop 0
	global_load_lds_dwordx4 v149, s[46:47]
	s_mov_b32 m0, s7
	s_nop 0
	s_mov_b32 s7, m0
	s_mov_b32 m0, s54
	s_nop 0
	global_load_lds_dwordx4 v1, s[42:43]
	s_mov_b32 m0, s7
	s_nop 0
	s_mov_b32 s7, m0
	s_mov_b32 m0, s60
	s_nop 0
	global_load_lds_dwordx4 v148, s[42:43]
	s_mov_b32 m0, s7
	s_waitcnt vmcnt(8)
	s_waitcnt lgkmcnt(0)
	s_barrier
	s_setprio 1
	s_waitcnt lgkmcnt(6)
	v_mfma_scale_f32_16x16x128_f8f6f4 v[64:67], v[132:139], v[68:75], v[64:67], v153, v153 op_sel_hi:[0,0,0]
	v_mfma_scale_f32_16x16x128_f8f6f4 v[60:63], v[156:163], v[68:75], v[60:63], v153, v153 op_sel_hi:[0,0,0]
	s_waitcnt lgkmcnt(4)
	v_mfma_scale_f32_16x16x128_f8f6f4 v[210:213], v[132:139], v[76:83], v[48:51], v153, v153 op_sel_hi:[0,0,0]
	v_mfma_scale_f32_16x16x128_f8f6f4 v[214:217], v[156:163], v[76:83], v[44:47], v153, v153 op_sel_hi:[0,0,0]
	s_waitcnt lgkmcnt(2)
	v_mfma_scale_f32_16x16x128_f8f6f4 v[218:221], v[132:139], v[84:91], v[32:35], v153, v153 op_sel_hi:[0,0,0]
	v_mfma_scale_f32_16x16x128_f8f6f4 v[222:225], v[156:163], v[84:91], v[28:31], v153, v153 op_sel_hi:[0,0,0]
	s_waitcnt lgkmcnt(0)
	v_mfma_scale_f32_16x16x128_f8f6f4 v[226:229], v[132:139], v[92:99], v[16:19], v153, v153 op_sel_hi:[0,0,0]
	v_mfma_scale_f32_16x16x128_f8f6f4 v[230:233], v[156:163], v[92:99], v[12:15], v153, v153 op_sel_hi:[0,0,0]
	s_setprio 0
	s_setprio 1
	v_mfma_scale_f32_16x16x128_f8f6f4 v[56:59], v[164:171], v[68:75], v[56:59], v153, v153 op_sel_hi:[0,0,0]
	v_mfma_scale_f32_16x16x128_f8f6f4 v[52:55], v[172:179], v[68:75], v[52:55], v153, v153 op_sel_hi:[0,0,0]
	v_mfma_scale_f32_16x16x128_f8f6f4 v[234:237], v[164:171], v[76:83], v[40:43], v153, v153 op_sel_hi:[0,0,0]
	v_mfma_scale_f32_16x16x128_f8f6f4 v[238:241], v[172:179], v[76:83], v[36:39], v153, v153 op_sel_hi:[0,0,0]
	v_mfma_scale_f32_16x16x128_f8f6f4 v[242:245], v[164:171], v[84:91], v[24:27], v153, v153 op_sel_hi:[0,0,0]
	v_mfma_scale_f32_16x16x128_f8f6f4 v[246:249], v[172:179], v[84:91], v[20:23], v153, v153 op_sel_hi:[0,0,0]
	v_mfma_scale_f32_16x16x128_f8f6f4 v[250:253], v[164:171], v[92:99], v[8:11], v153, v153 op_sel_hi:[0,0,0]
	v_mfma_scale_f32_16x16x128_f8f6f4 v[144:147], v[172:179], v[92:99], v[4:7], v153, v153 op_sel_hi:[0,0,0]
	s_setprio 0
	s_barrier
	s_nop 4
	ds_read_b128 v[4:7], v154
	ds_read_b128 v[8:11], v154 offset:1024
	ds_read_b128 v[20:23], v154 offset:2048
	ds_read_b128 v[24:27], v154 offset:3072
	ds_read_b128 v[132:135], v155
	ds_read_b128 v[136:139], v155 offset:1024
	ds_read_b128 v[156:159], v155 offset:2048
	ds_read_b128 v[160:163], v155 offset:3072
	ds_read_b128 v[12:15], v152 offset:32768
	ds_read_b128 v[16:19], v152 offset:33792
	ds_read_b128 v[28:31], v152 offset:34816
	ds_read_b128 v[32:35], v152 offset:35840
	ds_read_b128 v[36:39], v152 offset:36864
	ds_read_b128 v[40:43], v152 offset:37888
	ds_read_b128 v[44:47], v152 offset:38912
	ds_read_b128 v[48:51], v152 offset:39936
	s_add_u32 s42, s42, 0x40000
	s_addc_u32 s43, s43, 0
	s_mov_b32 s7, m0
	s_mov_b32 m0, s61
	s_nop 0
	global_load_lds_dwordx4 v1, s[42:43]
	s_mov_b32 m0, s7
	s_nop 0
	s_mov_b32 s7, m0
	s_mov_b32 m0, s64
	s_nop 0
	global_load_lds_dwordx4 v148, s[42:43]
	s_mov_b32 m0, s7
	s_waitcnt vmcnt(8)
	s_waitcnt lgkmcnt(0)
	s_barrier
	s_setprio 1
	s_waitcnt lgkmcnt(6)
	v_mfma_scale_f32_16x16x128_f8f6f4 v[128:131], v[4:11], v[12:19], v[128:131], v153, v153 op_sel_hi:[0,0,0]
	v_mfma_scale_f32_16x16x128_f8f6f4 v[124:127], v[20:27], v[12:19], v[124:127], v153, v153 op_sel_hi:[0,0,0]
	s_waitcnt lgkmcnt(4)
	v_mfma_scale_f32_16x16x128_f8f6f4 v[112:115], v[4:11], v[28:35], v[112:115], v153, v153 op_sel_hi:[0,0,0]
	v_mfma_scale_f32_16x16x128_f8f6f4 v[108:111], v[20:27], v[28:35], v[108:111], v153, v153 op_sel_hi:[0,0,0]
	s_waitcnt lgkmcnt(2)
	v_mfma_scale_f32_16x16x128_f8f6f4 v[96:99], v[4:11], v[36:43], v[140:143], v153, v153 op_sel_hi:[0,0,0]
	v_mfma_scale_f32_16x16x128_f8f6f4 v[92:95], v[20:27], v[36:43], v[188:191], v153, v153 op_sel_hi:[0,0,0]
	s_waitcnt lgkmcnt(0)
	v_mfma_scale_f32_16x16x128_f8f6f4 v[80:83], v[4:11], v[44:51], v[194:197], v153, v153 op_sel_hi:[0,0,0]
	v_mfma_scale_f32_16x16x128_f8f6f4 v[76:79], v[20:27], v[44:51], v[198:201], v153, v153 op_sel_hi:[0,0,0]
	s_setprio 0
	s_setprio 1
	v_mfma_scale_f32_16x16x128_f8f6f4 v[120:123], v[132:139], v[12:19], v[120:123], v153, v153 op_sel_hi:[0,0,0]
	v_mfma_scale_f32_16x16x128_f8f6f4 v[116:119], v[156:163], v[12:19], v[116:119], v153, v153 op_sel_hi:[0,0,0]
	v_mfma_scale_f32_16x16x128_f8f6f4 v[104:107], v[132:139], v[28:35], v[104:107], v153, v153 op_sel_hi:[0,0,0]
	v_mfma_scale_f32_16x16x128_f8f6f4 v[100:103], v[156:163], v[28:35], v[100:103], v153, v153 op_sel_hi:[0,0,0]
	v_mfma_scale_f32_16x16x128_f8f6f4 v[88:91], v[132:139], v[36:43], v[180:183], v153, v153 op_sel_hi:[0,0,0]
	v_mfma_scale_f32_16x16x128_f8f6f4 v[84:87], v[156:163], v[36:43], v[184:187], v153, v153 op_sel_hi:[0,0,0]
	v_mfma_scale_f32_16x16x128_f8f6f4 v[72:75], v[132:139], v[44:51], v[202:205], v153, v153 op_sel_hi:[0,0,0]
	v_mfma_scale_f32_16x16x128_f8f6f4 v[68:71], v[156:163], v[44:51], v[206:209], v153, v153 op_sel_hi:[0,0,0]
	s_setprio 0
	s_barrier
	ds_read_b128 v[36:39], v152 offset:49152
	ds_read_b128 v[40:43], v152 offset:50176
	ds_read_b128 v[164:167], v152 offset:51200
	ds_read_b128 v[168:171], v152 offset:52224
	ds_read_b128 v[172:175], v152 offset:53248
	ds_read_b128 v[176:179], v152 offset:54272
	ds_read_b128 v[180:183], v152 offset:55296
	ds_read_b128 v[184:187], v152 offset:56320
	s_add_u32 s42, s34, 0x80
	s_addc_u32 s43, s35, 0
	s_mov_b32 s7, m0
	s_mov_b32 m0, s73
	s_nop 0
	global_load_lds_dwordx4 v193, s[42:43]
	s_mov_b32 m0, s7
	s_add_u32 s34, s34, 0x40080
	s_mov_b32 s7, m0
	s_mov_b32 m0, s74
	s_nop 0
	global_load_lds_dwordx4 v149, s[42:43]
	s_mov_b32 m0, s7
	s_addc_u32 s35, s35, 0
	s_mov_b32 s7, m0
	s_mov_b32 m0, s78
	s_nop 0
	global_load_lds_dwordx4 v193, s[34:35]
	s_mov_b32 m0, s7
	s_nop 0
	s_mov_b32 s7, m0
	s_mov_b32 m0, s79
	s_nop 0
	global_load_lds_dwordx4 v149, s[34:35]
	s_mov_b32 m0, s7
	s_nop 0
	s_mov_b32 s7, m0
	s_mov_b32 m0, s75
	s_nop 0
	global_load_lds_dwordx4 v1, s[30:31]
	s_mov_b32 m0, s7
	s_nop 0
	s_mov_b32 s7, m0
	s_mov_b32 m0, s77
	s_nop 0
	global_load_lds_dwordx4 v148, s[30:31]
	s_mov_b32 m0, s7
	s_waitcnt vmcnt(8)
	s_waitcnt lgkmcnt(0)
	s_barrier
	s_setprio 1
	s_waitcnt lgkmcnt(6)
	v_mfma_scale_f32_16x16x128_f8f6f4 v[64:67], v[4:11], v[36:43], v[64:67], v153, v153 op_sel_hi:[0,0,0]
	v_mfma_scale_f32_16x16x128_f8f6f4 v[60:63], v[20:27], v[36:43], v[60:63], v153, v153 op_sel_hi:[0,0,0]
	s_waitcnt lgkmcnt(4)
	v_mfma_scale_f32_16x16x128_f8f6f4 v[48:51], v[4:11], v[164:171], v[210:213], v153, v153 op_sel_hi:[0,0,0]
	v_mfma_scale_f32_16x16x128_f8f6f4 v[44:47], v[20:27], v[164:171], v[214:217], v153, v153 op_sel_hi:[0,0,0]
	s_waitcnt lgkmcnt(2)
	v_mfma_scale_f32_16x16x128_f8f6f4 v[32:35], v[4:11], v[172:179], v[218:221], v153, v153 op_sel_hi:[0,0,0]
	v_mfma_scale_f32_16x16x128_f8f6f4 v[28:31], v[20:27], v[172:179], v[222:225], v153, v153 op_sel_hi:[0,0,0]
	s_waitcnt lgkmcnt(0)
	v_mfma_scale_f32_16x16x128_f8f6f4 v[16:19], v[4:11], v[180:187], v[226:229], v153, v153 op_sel_hi:[0,0,0]
	v_mfma_scale_f32_16x16x128_f8f6f4 v[12:15], v[20:27], v[180:187], v[230:233], v153, v153 op_sel_hi:[0,0,0]
	s_setprio 0
	s_setprio 1
	v_mfma_scale_f32_16x16x128_f8f6f4 v[56:59], v[132:139], v[36:43], v[56:59], v153, v153 op_sel_hi:[0,0,0]
	v_mfma_scale_f32_16x16x128_f8f6f4 v[52:55], v[156:163], v[36:43], v[52:55], v153, v153 op_sel_hi:[0,0,0]
	v_mfma_scale_f32_16x16x128_f8f6f4 v[40:43], v[132:139], v[164:171], v[234:237], v153, v153 op_sel_hi:[0,0,0]
	v_mfma_scale_f32_16x16x128_f8f6f4 v[36:39], v[156:163], v[164:171], v[238:241], v153, v153 op_sel_hi:[0,0,0]
	v_mfma_scale_f32_16x16x128_f8f6f4 v[24:27], v[132:139], v[172:179], v[242:245], v153, v153 op_sel_hi:[0,0,0]
	v_mfma_scale_f32_16x16x128_f8f6f4 v[20:23], v[156:163], v[172:179], v[246:249], v153, v153 op_sel_hi:[0,0,0]
	v_mfma_scale_f32_16x16x128_f8f6f4 v[8:11], v[132:139], v[180:187], v[250:253], v153, v153 op_sel_hi:[0,0,0]
	v_mfma_scale_f32_16x16x128_f8f6f4 v[4:7], v[156:163], v[180:187], v[144:147], v153, v153 op_sel_hi:[0,0,0]
	s_add_u32 s97, s97, 0x100
	s_addc_u32 vcc_lo, vcc_lo, 0
	s_add_u32 vcc_hi, vcc_hi, 0x100
	s_addc_u32 s53, s53, 0
	s_cmp_ge_i32 s44, s1
	s_mov_b32 s30, s44
	s_setprio 0
	s_barrier
	s_cbranch_scc0 .LBB0_1262
	v_readlane_b32 s95, v255, 9
	v_readlane_b32 s96, v255, 10
	s_and_b64 vcc, exec, s[8:9]
	s_cbranch_vccz .LBB0_1265

.LBB0_1587:
	ds_read_b128 v[144:147], v136
	ds_read_b128 v[148:151], v136 offset:1024
	ds_read_b128 v[152:155], v136 offset:2048
	ds_read_b128 v[156:159], v136 offset:3072
	ds_read_b128 v[160:163], v137
	ds_read_b128 v[164:167], v137 offset:1024
	ds_read_b128 v[168:171], v137 offset:2048
	ds_read_b128 v[172:175], v137 offset:3072
	s_add_i32 s82, s24, 2
	s_cmp_eq_u32 s77, s24
	s_cselect_b32 s28, s73, s78
	s_cselect_b32 s29, s72, s79
	s_cselect_b32 s26, s75, s80
	s_cselect_b32 s27, s74, s81
	s_add_u32 s24, s28, 0x80
	s_addc_u32 s25, s29, 0
	ds_read_b128 v[176:179], v138
	ds_read_b128 v[180:183], v138 offset:1024
	ds_read_b128 v[184:187], v138 offset:2048
	ds_read_b128 v[188:191], v138 offset:3072
	ds_read_b128 v[192:195], v138 offset:4096
	ds_read_b128 v[196:199], v138 offset:5120
	ds_read_b128 v[200:203], v138 offset:6144
	ds_read_b128 v[204:207], v138 offset:7168
	s_add_u32 s84, s78, 0x7ff80
	s_addc_u32 s85, s79, 0
	s_mov_b32 s83, m0
	s_mov_b32 m0, s57
	s_nop 0
	global_load_lds_dwordx4 v132, s[84:85]
	s_mov_b32 m0, s83
	s_nop 0
	s_mov_b32 s83, m0
	s_mov_b32 m0, s58
	s_nop 0
	global_load_lds_dwordx4 v134, s[84:85]
	s_mov_b32 m0, s83
	s_waitcnt vmcnt(8)
	s_waitcnt lgkmcnt(0)
	s_barrier
	s_setprio 1
	s_waitcnt lgkmcnt(7)
	v_mfma_f32_16x16x32_bf16 v[126:129], v[144:147], v[176:179], v[126:129]
	v_mfma_f32_16x16x32_bf16 v[122:125], v[152:155], v[176:179], v[122:125]
	s_waitcnt lgkmcnt(5)
	v_mfma_f32_16x16x32_bf16 v[110:113], v[144:147], v[184:187], v[110:113]
	v_mfma_f32_16x16x32_bf16 v[106:109], v[152:155], v[184:187], v[106:109]
	s_waitcnt lgkmcnt(3)
	v_mfma_f32_16x16x32_bf16 v[94:97], v[144:147], v[192:195], v[94:97]
	v_mfma_f32_16x16x32_bf16 v[90:93], v[152:155], v[192:195], v[90:93]
	s_waitcnt lgkmcnt(1)
	v_mfma_f32_16x16x32_bf16 v[78:81], v[144:147], v[200:203], v[78:81]
	v_mfma_f32_16x16x32_bf16 v[74:77], v[152:155], v[200:203], v[74:77]
	v_mfma_f32_16x16x32_bf16 v[126:129], v[148:151], v[180:183], v[126:129]
	v_mfma_f32_16x16x32_bf16 v[122:125], v[156:159], v[180:183], v[122:125]
	v_mfma_f32_16x16x32_bf16 v[110:113], v[148:151], v[188:191], v[110:113]
	v_mfma_f32_16x16x32_bf16 v[106:109], v[156:159], v[188:191], v[106:109]
	v_mfma_f32_16x16x32_bf16 v[94:97], v[148:151], v[196:199], v[94:97]
	v_mfma_f32_16x16x32_bf16 v[90:93], v[156:159], v[196:199], v[90:93]
	s_waitcnt lgkmcnt(0)
	v_mfma_f32_16x16x32_bf16 v[78:81], v[148:151], v[204:207], v[78:81]
	v_mfma_f32_16x16x32_bf16 v[74:77], v[156:159], v[204:207], v[74:77]
	s_setprio 0
	s_setprio 1
	v_mfma_f32_16x16x32_bf16 v[118:121], v[160:163], v[176:179], v[118:121]
	v_mfma_f32_16x16x32_bf16 v[114:117], v[168:171], v[176:179], v[114:117]
	v_mfma_f32_16x16x32_bf16 v[102:105], v[160:163], v[184:187], v[102:105]
	v_mfma_f32_16x16x32_bf16 v[98:101], v[168:171], v[184:187], v[98:101]
	v_mfma_f32_16x16x32_bf16 v[86:89], v[160:163], v[192:195], v[86:89]
	v_mfma_f32_16x16x32_bf16 v[82:85], v[168:171], v[192:195], v[82:85]
	v_mfma_f32_16x16x32_bf16 v[70:73], v[160:163], v[200:203], v[70:73]
	v_mfma_f32_16x16x32_bf16 v[66:69], v[168:171], v[200:203], v[66:69]
	v_mfma_f32_16x16x32_bf16 v[118:121], v[164:167], v[180:183], v[118:121]
	v_mfma_f32_16x16x32_bf16 v[114:117], v[172:175], v[180:183], v[114:117]
	v_mfma_f32_16x16x32_bf16 v[102:105], v[164:167], v[188:191], v[102:105]
	v_mfma_f32_16x16x32_bf16 v[98:101], v[172:175], v[188:191], v[98:101]
	v_mfma_f32_16x16x32_bf16 v[86:89], v[164:167], v[196:199], v[86:89]
	v_mfma_f32_16x16x32_bf16 v[82:85], v[172:175], v[196:199], v[82:85]
	v_mfma_f32_16x16x32_bf16 v[70:73], v[164:167], v[204:207], v[70:73]
	v_mfma_f32_16x16x32_bf16 v[66:69], v[172:175], v[204:207], v[66:69]
	s_setprio 0
	s_barrier
	ds_read_b128 v[176:179], v138 offset:16384
	ds_read_b128 v[180:183], v138 offset:17408
	ds_read_b128 v[184:187], v138 offset:18432
	ds_read_b128 v[188:191], v138 offset:19456
	ds_read_b128 v[192:195], v138 offset:20480
	ds_read_b128 v[196:199], v138 offset:21504
	ds_read_b128 v[200:203], v138 offset:22528
	ds_read_b128 v[204:207], v138 offset:23552
	s_mov_b32 s83, m0
	s_mov_b32 m0, s37
	s_nop 0
	global_load_lds_dwordx4 v133, s[26:27]
	s_mov_b32 m0, s83
	s_add_u32 s84, s26, 0x20000
	s_mov_b32 s83, m0
	s_mov_b32 m0, s38
	s_nop 0
	global_load_lds_dwordx4 v135, s[26:27]
	s_mov_b32 m0, s83
	s_addc_u32 s85, s27, 0
	s_mov_b32 s83, m0
	s_mov_b32 m0, s39
	s_nop 0
	global_load_lds_dwordx4 v133, s[84:85]
	s_mov_b32 m0, s83
	s_nop 0
	s_mov_b32 s83, m0
	s_mov_b32 m0, s40
	s_nop 0
	global_load_lds_dwordx4 v135, s[84:85]
	s_mov_b32 m0, s83
	s_nop 0
	s_mov_b32 s83, m0
	s_mov_b32 m0, s36
	s_nop 0
	global_load_lds_dwordx4 v132, s[28:29]
	s_mov_b32 m0, s83
	s_nop 0
	s_mov_b32 s83, m0
	s_mov_b32 m0, s42
	s_nop 0
	global_load_lds_dwordx4 v134, s[28:29]
	s_mov_b32 m0, s83
	s_waitcnt vmcnt(8)
	s_waitcnt lgkmcnt(0)
	s_barrier
	s_setprio 1
	s_waitcnt lgkmcnt(7)
	v_mfma_f32_16x16x32_bf16 v[62:65], v[144:147], v[176:179], v[62:65]
	v_mfma_f32_16x16x32_bf16 v[58:61], v[152:155], v[176:179], v[58:61]
	s_waitcnt lgkmcnt(5)
	v_mfma_f32_16x16x32_bf16 v[46:49], v[144:147], v[184:187], v[46:49]
	v_mfma_f32_16x16x32_bf16 v[42:45], v[152:155], v[184:187], v[42:45]
	s_waitcnt lgkmcnt(3)
	v_mfma_f32_16x16x32_bf16 v[30:33], v[144:147], v[192:195], v[30:33]
	v_mfma_f32_16x16x32_bf16 v[26:29], v[152:155], v[192:195], v[26:29]
	s_waitcnt lgkmcnt(1)
	v_mfma_f32_16x16x32_bf16 v[14:17], v[144:147], v[200:203], v[14:17]
	v_mfma_f32_16x16x32_bf16 v[10:13], v[152:155], v[200:203], v[10:13]
	v_mfma_f32_16x16x32_bf16 v[62:65], v[148:151], v[180:183], v[62:65]
	v_mfma_f32_16x16x32_bf16 v[58:61], v[156:159], v[180:183], v[58:61]
	v_mfma_f32_16x16x32_bf16 v[46:49], v[148:151], v[188:191], v[46:49]
	v_mfma_f32_16x16x32_bf16 v[42:45], v[156:159], v[188:191], v[42:45]
	v_mfma_f32_16x16x32_bf16 v[30:33], v[148:151], v[196:199], v[30:33]
	v_mfma_f32_16x16x32_bf16 v[26:29], v[156:159], v[196:199], v[26:29]
	s_waitcnt lgkmcnt(0)
	v_mfma_f32_16x16x32_bf16 v[14:17], v[148:151], v[204:207], v[14:17]
	v_mfma_f32_16x16x32_bf16 v[10:13], v[156:159], v[204:207], v[10:13]
	s_setprio 0
	s_setprio 1
	v_mfma_f32_16x16x32_bf16 v[54:57], v[160:163], v[176:179], v[54:57]
	v_mfma_f32_16x16x32_bf16 v[50:53], v[168:171], v[176:179], v[50:53]
	v_mfma_f32_16x16x32_bf16 v[38:41], v[160:163], v[184:187], v[38:41]
	v_mfma_f32_16x16x32_bf16 v[34:37], v[168:171], v[184:187], v[34:37]
	v_mfma_f32_16x16x32_bf16 v[22:25], v[160:163], v[192:195], v[22:25]
	v_mfma_f32_16x16x32_bf16 v[18:21], v[168:171], v[192:195], v[18:21]
	v_mfma_f32_16x16x32_bf16 v[6:9], v[160:163], v[200:203], v[6:9]
	v_mfma_f32_16x16x32_bf16 v[2:5], v[168:171], v[200:203], v[2:5]
	v_mfma_f32_16x16x32_bf16 v[54:57], v[164:167], v[180:183], v[54:57]
	v_mfma_f32_16x16x32_bf16 v[50:53], v[172:175], v[180:183], v[50:53]
	v_mfma_f32_16x16x32_bf16 v[38:41], v[164:167], v[188:191], v[38:41]
	v_mfma_f32_16x16x32_bf16 v[34:37], v[172:175], v[188:191], v[34:37]
	v_mfma_f32_16x16x32_bf16 v[22:25], v[164:167], v[196:199], v[22:25]
	v_mfma_f32_16x16x32_bf16 v[18:21], v[172:175], v[196:199], v[18:21]
	v_mfma_f32_16x16x32_bf16 v[6:9], v[164:167], v[204:207], v[6:9]
	v_mfma_f32_16x16x32_bf16 v[2:5], v[172:175], v[204:207], v[2:5]
	s_setprio 0
	s_barrier
	ds_read_b128 v[144:147], v139
	ds_read_b128 v[148:151], v139 offset:1024
	ds_read_b128 v[152:155], v139 offset:2048
	ds_read_b128 v[156:159], v139 offset:3072
	ds_read_b128 v[160:163], v140
	ds_read_b128 v[164:167], v140 offset:1024
	ds_read_b128 v[168:171], v140 offset:2048
	ds_read_b128 v[172:175], v140 offset:3072
	ds_read_b128 v[176:179], v138 offset:32768
	ds_read_b128 v[180:183], v138 offset:33792
	ds_read_b128 v[184:187], v138 offset:34816
	ds_read_b128 v[188:191], v138 offset:35840
	ds_read_b128 v[192:195], v138 offset:36864
	ds_read_b128 v[196:199], v138 offset:37888
	ds_read_b128 v[200:203], v138 offset:38912
	ds_read_b128 v[204:207], v138 offset:39936
	s_add_u32 s28, s28, 0x80000
	s_addc_u32 s29, s29, 0
	s_mov_b32 s83, m0
	s_mov_b32 m0, s43
	s_nop 0
	global_load_lds_dwordx4 v132, s[28:29]
	s_mov_b32 m0, s83
	s_nop 0
	s_mov_b32 s83, m0
	s_mov_b32 m0, s44
	s_nop 0
	global_load_lds_dwordx4 v134, s[28:29]
	s_mov_b32 m0, s83
	s_waitcnt vmcnt(8)
	s_waitcnt lgkmcnt(0)
	s_barrier
	s_setprio 1
	s_waitcnt lgkmcnt(7)
	v_mfma_f32_16x16x32_bf16 v[126:129], v[144:147], v[176:179], v[126:129]
	v_mfma_f32_16x16x32_bf16 v[122:125], v[152:155], v[176:179], v[122:125]
	s_waitcnt lgkmcnt(5)
	v_mfma_f32_16x16x32_bf16 v[110:113], v[144:147], v[184:187], v[110:113]
	v_mfma_f32_16x16x32_bf16 v[106:109], v[152:155], v[184:187], v[106:109]
	s_waitcnt lgkmcnt(3)
	v_mfma_f32_16x16x32_bf16 v[94:97], v[144:147], v[192:195], v[94:97]
	v_mfma_f32_16x16x32_bf16 v[90:93], v[152:155], v[192:195], v[90:93]
	s_waitcnt lgkmcnt(1)
	v_mfma_f32_16x16x32_bf16 v[78:81], v[144:147], v[200:203], v[78:81]
	v_mfma_f32_16x16x32_bf16 v[74:77], v[152:155], v[200:203], v[74:77]
	v_mfma_f32_16x16x32_bf16 v[126:129], v[148:151], v[180:183], v[126:129]
	v_mfma_f32_16x16x32_bf16 v[122:125], v[156:159], v[180:183], v[122:125]
	v_mfma_f32_16x16x32_bf16 v[110:113], v[148:151], v[188:191], v[110:113]
	v_mfma_f32_16x16x32_bf16 v[106:109], v[156:159], v[188:191], v[106:109]
	v_mfma_f32_16x16x32_bf16 v[94:97], v[148:151], v[196:199], v[94:97]
	v_mfma_f32_16x16x32_bf16 v[90:93], v[156:159], v[196:199], v[90:93]
	s_waitcnt lgkmcnt(0)
	v_mfma_f32_16x16x32_bf16 v[78:81], v[148:151], v[204:207], v[78:81]
	v_mfma_f32_16x16x32_bf16 v[74:77], v[156:159], v[204:207], v[74:77]
	s_setprio 0
	s_setprio 1
	v_mfma_f32_16x16x32_bf16 v[118:121], v[160:163], v[176:179], v[118:121]
	v_mfma_f32_16x16x32_bf16 v[114:117], v[168:171], v[176:179], v[114:117]
	v_mfma_f32_16x16x32_bf16 v[102:105], v[160:163], v[184:187], v[102:105]
	v_mfma_f32_16x16x32_bf16 v[98:101], v[168:171], v[184:187], v[98:101]
	v_mfma_f32_16x16x32_bf16 v[86:89], v[160:163], v[192:195], v[86:89]
	v_mfma_f32_16x16x32_bf16 v[82:85], v[168:171], v[192:195], v[82:85]
	v_mfma_f32_16x16x32_bf16 v[70:73], v[160:163], v[200:203], v[70:73]
	v_mfma_f32_16x16x32_bf16 v[66:69], v[168:171], v[200:203], v[66:69]
	v_mfma_f32_16x16x32_bf16 v[118:121], v[164:167], v[180:183], v[118:121]
	v_mfma_f32_16x16x32_bf16 v[114:117], v[172:175], v[180:183], v[114:117]
	v_mfma_f32_16x16x32_bf16 v[102:105], v[164:167], v[188:191], v[102:105]
	v_mfma_f32_16x16x32_bf16 v[98:101], v[172:175], v[188:191], v[98:101]
	v_mfma_f32_16x16x32_bf16 v[86:89], v[164:167], v[196:199], v[86:89]
	v_mfma_f32_16x16x32_bf16 v[82:85], v[172:175], v[196:199], v[82:85]
	v_mfma_f32_16x16x32_bf16 v[70:73], v[164:167], v[204:207], v[70:73]
	v_mfma_f32_16x16x32_bf16 v[66:69], v[172:175], v[204:207], v[66:69]
	s_setprio 0
	s_barrier
	ds_read_b128 v[176:179], v138 offset:49152
	ds_read_b128 v[180:183], v138 offset:50176
	ds_read_b128 v[184:187], v138 offset:51200
	ds_read_b128 v[188:191], v138 offset:52224
	ds_read_b128 v[192:195], v138 offset:53248
	ds_read_b128 v[196:199], v138 offset:54272
	ds_read_b128 v[200:203], v138 offset:55296
	ds_read_b128 v[204:207], v138 offset:56320
	s_add_u32 s28, s26, 0x80
	s_addc_u32 s29, s27, 0
	s_mov_b32 s83, m0
	s_mov_b32 m0, s47
	s_nop 0
	global_load_lds_dwordx4 v133, s[28:29]
	s_mov_b32 m0, s83
	s_add_u32 s26, s26, 0x20080
	s_mov_b32 s83, m0
	s_mov_b32 m0, s52
	s_nop 0
	global_load_lds_dwordx4 v135, s[28:29]
	s_mov_b32 m0, s83
	s_addc_u32 s27, s27, 0
	s_mov_b32 s28, m0
	s_mov_b32 m0, s55
	s_nop 0
	global_load_lds_dwordx4 v133, s[26:27]
	s_mov_b32 m0, s28
	s_nop 0
	s_mov_b32 s28, m0
	s_mov_b32 m0, s56
	s_nop 0
	global_load_lds_dwordx4 v135, s[26:27]
	s_mov_b32 m0, s28
	s_mov_b32 s26, m0
	s_mov_b32 m0, s53
	s_nop 0
	global_load_lds_dwordx4 v132, s[24:25]
	s_mov_b32 m0, s26
	s_nop 0
	s_mov_b32 s26, m0
	s_mov_b32 m0, s54
	s_nop 0
	global_load_lds_dwordx4 v134, s[24:25]
	s_mov_b32 m0, s26
	s_waitcnt vmcnt(8)
	s_waitcnt lgkmcnt(0)
	s_barrier
	s_setprio 1
	s_waitcnt lgkmcnt(7)
	v_mfma_f32_16x16x32_bf16 v[62:65], v[144:147], v[176:179], v[62:65]
	v_mfma_f32_16x16x32_bf16 v[58:61], v[152:155], v[176:179], v[58:61]
	s_waitcnt lgkmcnt(5)
	v_mfma_f32_16x16x32_bf16 v[46:49], v[144:147], v[184:187], v[46:49]
	v_mfma_f32_16x16x32_bf16 v[42:45], v[152:155], v[184:187], v[42:45]
	s_waitcnt lgkmcnt(3)
	v_mfma_f32_16x16x32_bf16 v[30:33], v[144:147], v[192:195], v[30:33]
	v_mfma_f32_16x16x32_bf16 v[26:29], v[152:155], v[192:195], v[26:29]
	s_waitcnt lgkmcnt(1)
	v_mfma_f32_16x16x32_bf16 v[14:17], v[144:147], v[200:203], v[14:17]
	v_mfma_f32_16x16x32_bf16 v[10:13], v[152:155], v[200:203], v[10:13]
	v_mfma_f32_16x16x32_bf16 v[62:65], v[148:151], v[180:183], v[62:65]
	v_mfma_f32_16x16x32_bf16 v[58:61], v[156:159], v[180:183], v[58:61]
	v_mfma_f32_16x16x32_bf16 v[46:49], v[148:151], v[188:191], v[46:49]
	v_mfma_f32_16x16x32_bf16 v[42:45], v[156:159], v[188:191], v[42:45]
	v_mfma_f32_16x16x32_bf16 v[30:33], v[148:151], v[196:199], v[30:33]
	v_mfma_f32_16x16x32_bf16 v[26:29], v[156:159], v[196:199], v[26:29]
	s_waitcnt lgkmcnt(0)
	v_mfma_f32_16x16x32_bf16 v[14:17], v[148:151], v[204:207], v[14:17]
	v_mfma_f32_16x16x32_bf16 v[10:13], v[156:159], v[204:207], v[10:13]
	s_setprio 0
	s_setprio 1
	v_mfma_f32_16x16x32_bf16 v[54:57], v[160:163], v[176:179], v[54:57]
	v_mfma_f32_16x16x32_bf16 v[50:53], v[168:171], v[176:179], v[50:53]
	v_mfma_f32_16x16x32_bf16 v[38:41], v[160:163], v[184:187], v[38:41]
	v_mfma_f32_16x16x32_bf16 v[34:37], v[168:171], v[184:187], v[34:37]
	v_mfma_f32_16x16x32_bf16 v[22:25], v[160:163], v[192:195], v[22:25]
	v_mfma_f32_16x16x32_bf16 v[18:21], v[168:171], v[192:195], v[18:21]
	v_mfma_f32_16x16x32_bf16 v[6:9], v[160:163], v[200:203], v[6:9]
	v_mfma_f32_16x16x32_bf16 v[2:5], v[168:171], v[200:203], v[2:5]
	v_mfma_f32_16x16x32_bf16 v[54:57], v[164:167], v[180:183], v[54:57]
	v_mfma_f32_16x16x32_bf16 v[50:53], v[172:175], v[180:183], v[50:53]
	v_mfma_f32_16x16x32_bf16 v[38:41], v[164:167], v[188:191], v[38:41]
	v_mfma_f32_16x16x32_bf16 v[34:37], v[172:175], v[188:191], v[34:37]
	v_mfma_f32_16x16x32_bf16 v[22:25], v[164:167], v[196:199], v[22:25]
	v_mfma_f32_16x16x32_bf16 v[18:21], v[172:175], v[196:199], v[18:21]
	v_mfma_f32_16x16x32_bf16 v[6:9], v[164:167], v[204:207], v[6:9]
	v_mfma_f32_16x16x32_bf16 v[2:5], v[172:175], v[204:207], v[2:5]
	s_add_u32 s78, s78, 0x100
	s_addc_u32 s79, s79, 0
	s_add_u32 s80, s80, 0x100
	s_addc_u32 s81, s81, 0
	s_cmp_ge_i32 s82, s69
	s_mov_b32 s24, s82
	s_setprio 0
	s_barrier
	s_cbranch_scc0 .LBB0_1587
	s_and_b64 vcc, exec, s[2:3]
	s_cbranch_vccz .LBB0_1590

.LBB0_1676:
	v_add_u32_e32 v1, 0x10000, v170
	ds_read_b128 v[38:41], v1
	ds_read_b128 v[42:45], v1 offset:1024
	ds_read_b128 v[70:73], v1 offset:2048
	ds_read_b128 v[74:77], v1 offset:3072
	v_add_u32_e32 v1, 0x14000, v170
	ds_read_b128 v[102:105], v1
	ds_read_b128 v[106:109], v1 offset:1024
	ds_read_b128 v[134:137], v1 offset:2048
	ds_read_b128 v[138:141], v1 offset:3072
	s_add_i32 s89, s40, 2
	s_cmp_eq_u32 s84, s40
	s_cselect_b32 s44, s81, s85
	s_cselect_b32 s45, s80, s86
	s_cselect_b32 s42, s83, s87
	s_cselect_b32 s43, s82, s88
	s_add_u32 s40, s44, 0x80
	s_addc_u32 s41, s45, 0
	ds_read_b128 v[174:177], v171
	ds_read_b128 v[178:181], v171 offset:1024
	ds_read_b128 v[182:185], v171 offset:2048
	ds_read_b128 v[186:189], v171 offset:3072
	ds_read_b128 v[190:193], v171 offset:4096
	ds_read_b128 v[194:197], v171 offset:5120
	ds_read_b128 v[202:205], v171 offset:6144
	ds_read_b128 v[206:209], v171 offset:7168
	s_add_u32 s90, s85, 0x3ff80
	s_addc_u32 s91, s86, 0
	s_mov_b32 s92, m0
	s_mov_b32 m0, s72
	s_nop 0
	global_load_lds_dwordx4 v166, s[90:91]
	s_mov_b32 m0, s92
	s_nop 0
	s_mov_b32 s92, m0
	s_mov_b32 m0, s73
	s_nop 0
	global_load_lds_dwordx4 v168, s[90:91]
	s_mov_b32 m0, s92
	s_waitcnt vmcnt(8)
	s_waitcnt lgkmcnt(0)
	s_barrier
	s_setprio 1
	s_waitcnt lgkmcnt(0)
	v_mfma_scale_f32_16x16x128_f8f6f4 v[130:133], v[38:45], v[202:209], v[130:133], v172, v172 op_sel_hi:[0,0,0]
	v_mfma_scale_f32_16x16x128_f8f6f4 v[126:129], v[70:77], v[202:209], v[126:129], v172, v172 op_sel_hi:[0,0,0]
	v_mfma_scale_f32_16x16x128_f8f6f4 v[198:201], v[38:45], v[174:181], v[58:61], v172, v172 op_sel_hi:[0,0,0]
	v_mfma_scale_f32_16x16x128_f8f6f4 v[210:213], v[70:77], v[174:181], v[54:57], v172, v172 op_sel_hi:[0,0,0]
	v_mfma_scale_f32_16x16x128_f8f6f4 v[214:217], v[38:45], v[182:189], v[90:93], v172, v172 op_sel_hi:[0,0,0]
	v_mfma_scale_f32_16x16x128_f8f6f4 v[218:221], v[70:77], v[182:189], v[86:89], v172, v172 op_sel_hi:[0,0,0]
	v_mfma_scale_f32_16x16x128_f8f6f4 v[222:225], v[38:45], v[190:197], v[122:125], v172, v172 op_sel_hi:[0,0,0]
	v_mfma_scale_f32_16x16x128_f8f6f4 v[226:229], v[70:77], v[190:197], v[118:121], v172, v172 op_sel_hi:[0,0,0]
	s_setprio 0
	s_setprio 1
	v_mfma_scale_f32_16x16x128_f8f6f4 v[162:165], v[102:109], v[174:181], v[162:165], v172, v172 op_sel_hi:[0,0,0]
	v_mfma_scale_f32_16x16x128_f8f6f4 v[158:161], v[134:141], v[174:181], v[158:161], v172, v172 op_sel_hi:[0,0,0]
	v_mfma_scale_f32_16x16x128_f8f6f4 v[154:157], v[102:109], v[182:189], v[154:157], v172, v172 op_sel_hi:[0,0,0]
	v_mfma_scale_f32_16x16x128_f8f6f4 v[150:153], v[134:141], v[182:189], v[150:153], v172, v172 op_sel_hi:[0,0,0]
	v_mfma_scale_f32_16x16x128_f8f6f4 v[146:149], v[102:109], v[190:197], v[146:149], v172, v172 op_sel_hi:[0,0,0]
	v_mfma_scale_f32_16x16x128_f8f6f4 v[142:145], v[134:141], v[190:197], v[142:145], v172, v172 op_sel_hi:[0,0,0]
	v_mfma_scale_f32_16x16x128_f8f6f4 v[174:177], v[102:109], v[202:209], v[114:117], v172, v172 op_sel_hi:[0,0,0]
	v_mfma_scale_f32_16x16x128_f8f6f4 v[178:181], v[134:141], v[202:209], v[110:113], v172, v172 op_sel_hi:[0,0,0]
	s_setprio 0
	s_barrier
	ds_read_b128 v[54:57], v171 offset:16384
	ds_read_b128 v[58:61], v171 offset:17408
	ds_read_b128 v[86:89], v171 offset:18432
	ds_read_b128 v[90:93], v171 offset:19456
	s_nop 0
	ds_read_b128 v[110:113], v171 offset:20480
	ds_read_b128 v[114:117], v171 offset:21504
	ds_read_b128 v[118:121], v171 offset:22528
	ds_read_b128 v[122:125], v171 offset:23552
	s_mov_b32 s90, m0
	s_mov_b32 m0, s52
	s_nop 0
	global_load_lds_dwordx4 v167, s[42:43]
	s_mov_b32 m0, s90
	s_nop 0
	s_mov_b32 s90, m0
	s_mov_b32 m0, s53
	s_nop 0
	global_load_lds_dwordx4 v169, s[42:43]
	s_mov_b32 m0, s90
	s_add_u32 s90, s42, 0x40000
	s_addc_u32 s91, s43, 0
	s_mov_b32 s92, m0
	s_mov_b32 m0, s54
	s_nop 0
	global_load_lds_dwordx4 v167, s[90:91]
	s_mov_b32 m0, s92
	s_nop 0
	s_mov_b32 s92, m0
	s_mov_b32 m0, s55
	s_nop 0
	global_load_lds_dwordx4 v169, s[90:91]
	s_mov_b32 m0, s92
	s_mov_b32 s90, m0
	s_mov_b32 m0, s7
	s_nop 0
	global_load_lds_dwordx4 v166, s[44:45]
	s_mov_b32 m0, s90
	s_nop 0
	s_mov_b32 s90, m0
	s_mov_b32 m0, s56
	s_nop 0
	global_load_lds_dwordx4 v168, s[44:45]
	s_mov_b32 m0, s90
	s_waitcnt vmcnt(8)
	s_waitcnt lgkmcnt(0)
	s_barrier
	s_setprio 1
	s_waitcnt lgkmcnt(6)
	v_mfma_scale_f32_16x16x128_f8f6f4 v[98:101], v[38:45], v[54:61], v[98:101], v172, v172 op_sel_hi:[0,0,0]
	v_mfma_scale_f32_16x16x128_f8f6f4 v[94:97], v[70:77], v[54:61], v[94:97], v172, v172 op_sel_hi:[0,0,0]
	s_waitcnt lgkmcnt(4)
	v_mfma_scale_f32_16x16x128_f8f6f4 v[182:185], v[38:45], v[86:93], v[66:69], v172, v172 op_sel_hi:[0,0,0]
	v_mfma_scale_f32_16x16x128_f8f6f4 v[186:189], v[70:77], v[86:93], v[62:65], v172, v172 op_sel_hi:[0,0,0]
	s_waitcnt lgkmcnt(2)
	v_mfma_scale_f32_16x16x128_f8f6f4 v[190:193], v[38:45], v[110:117], v[34:37], v172, v172 op_sel_hi:[0,0,0]
	v_mfma_scale_f32_16x16x128_f8f6f4 v[194:197], v[70:77], v[110:117], v[30:33], v172, v172 op_sel_hi:[0,0,0]
	s_waitcnt lgkmcnt(0)
	v_mfma_scale_f32_16x16x128_f8f6f4 v[202:205], v[38:45], v[118:125], v[18:21], v172, v172 op_sel_hi:[0,0,0]
	v_mfma_scale_f32_16x16x128_f8f6f4 v[206:209], v[70:77], v[118:125], v[14:17], v172, v172 op_sel_hi:[0,0,0]
	s_setprio 0
	s_setprio 1
	v_mfma_scale_f32_16x16x128_f8f6f4 v[82:85], v[102:109], v[54:61], v[82:85], v172, v172 op_sel_hi:[0,0,0]
	v_mfma_scale_f32_16x16x128_f8f6f4 v[78:81], v[134:141], v[54:61], v[78:81], v172, v172 op_sel_hi:[0,0,0]
	v_mfma_scale_f32_16x16x128_f8f6f4 v[230:233], v[102:109], v[86:93], v[50:53], v172, v172 op_sel_hi:[0,0,0]
	v_mfma_scale_f32_16x16x128_f8f6f4 v[234:237], v[134:141], v[86:93], v[46:49], v172, v172 op_sel_hi:[0,0,0]
	v_mfma_scale_f32_16x16x128_f8f6f4 v[238:241], v[102:109], v[110:117], v[26:29], v172, v172 op_sel_hi:[0,0,0]
	v_mfma_scale_f32_16x16x128_f8f6f4 v[242:245], v[134:141], v[110:117], v[22:25], v172, v172 op_sel_hi:[0,0,0]
	v_mfma_scale_f32_16x16x128_f8f6f4 v[246:249], v[102:109], v[118:125], v[10:13], v172, v172 op_sel_hi:[0,0,0]
	v_mfma_scale_f32_16x16x128_f8f6f4 v[250:253], v[134:141], v[118:125], v[6:9], v172, v172 op_sel_hi:[0,0,0]
	s_setprio 0
	s_barrier
	v_add_u32_e32 v1, 0x18000, v170
	s_nop 3
	ds_read_b128 v[4:7], v1
	ds_read_b128 v[8:11], v1 offset:1024
	ds_read_b128 v[22:25], v1 offset:2048
	ds_read_b128 v[26:29], v1 offset:3072
	v_add_u32_e32 v1, 0x1c000, v170
	ds_read_b128 v[38:41], v1
	ds_read_b128 v[42:45], v1 offset:1024
	ds_read_b128 v[70:73], v1 offset:2048
	ds_read_b128 v[74:77], v1 offset:3072
	ds_read_b128 v[12:15], v171 offset:32768
	ds_read_b128 v[16:19], v171 offset:33792
	ds_read_b128 v[30:33], v171 offset:34816
	ds_read_b128 v[34:37], v171 offset:35840
	ds_read_b128 v[46:49], v171 offset:36864
	ds_read_b128 v[50:53], v171 offset:37888
	ds_read_b128 v[62:65], v171 offset:38912
	ds_read_b128 v[66:69], v171 offset:39936
	s_add_u32 s44, s44, 0x40000
	s_addc_u32 s45, s45, 0
	s_mov_b32 s90, m0
	s_mov_b32 m0, s57
	s_nop 0
	global_load_lds_dwordx4 v166, s[44:45]
	s_mov_b32 m0, s90
	s_nop 0
	s_mov_b32 s90, m0
	s_mov_b32 m0, s58
	s_nop 0
	global_load_lds_dwordx4 v168, s[44:45]
	s_mov_b32 m0, s90
	s_waitcnt vmcnt(8)
	s_waitcnt lgkmcnt(0)
	s_barrier
	s_setprio 1
	s_waitcnt lgkmcnt(6)
	v_mfma_scale_f32_16x16x128_f8f6f4 v[58:61], v[4:11], v[12:19], v[198:201], v172, v172 op_sel_hi:[0,0,0]
	v_mfma_scale_f32_16x16x128_f8f6f4 v[54:57], v[22:29], v[12:19], v[210:213], v172, v172 op_sel_hi:[0,0,0]
	s_waitcnt lgkmcnt(4)
	v_mfma_scale_f32_16x16x128_f8f6f4 v[90:93], v[4:11], v[30:37], v[214:217], v172, v172 op_sel_hi:[0,0,0]
	v_mfma_scale_f32_16x16x128_f8f6f4 v[86:89], v[22:29], v[30:37], v[218:221], v172, v172 op_sel_hi:[0,0,0]
	s_waitcnt lgkmcnt(2)
	v_mfma_scale_f32_16x16x128_f8f6f4 v[122:125], v[4:11], v[46:53], v[222:225], v172, v172 op_sel_hi:[0,0,0]
	v_mfma_scale_f32_16x16x128_f8f6f4 v[118:121], v[22:29], v[46:53], v[226:229], v172, v172 op_sel_hi:[0,0,0]
	s_waitcnt lgkmcnt(0)
	v_mfma_scale_f32_16x16x128_f8f6f4 v[130:133], v[4:11], v[62:69], v[130:133], v172, v172 op_sel_hi:[0,0,0]
	v_mfma_scale_f32_16x16x128_f8f6f4 v[126:129], v[22:29], v[62:69], v[126:129], v172, v172 op_sel_hi:[0,0,0]
	s_setprio 0
	s_setprio 1
	v_mfma_scale_f32_16x16x128_f8f6f4 v[162:165], v[38:45], v[12:19], v[162:165], v172, v172 op_sel_hi:[0,0,0]
	v_mfma_scale_f32_16x16x128_f8f6f4 v[158:161], v[70:77], v[12:19], v[158:161], v172, v172 op_sel_hi:[0,0,0]
	v_mfma_scale_f32_16x16x128_f8f6f4 v[154:157], v[38:45], v[30:37], v[154:157], v172, v172 op_sel_hi:[0,0,0]
	v_mfma_scale_f32_16x16x128_f8f6f4 v[150:153], v[70:77], v[30:37], v[150:153], v172, v172 op_sel_hi:[0,0,0]
	v_mfma_scale_f32_16x16x128_f8f6f4 v[146:149], v[38:45], v[46:53], v[146:149], v172, v172 op_sel_hi:[0,0,0]
	v_mfma_scale_f32_16x16x128_f8f6f4 v[142:145], v[70:77], v[46:53], v[142:145], v172, v172 op_sel_hi:[0,0,0]
	v_mfma_scale_f32_16x16x128_f8f6f4 v[114:117], v[38:45], v[62:69], v[174:177], v172, v172 op_sel_hi:[0,0,0]
	v_mfma_scale_f32_16x16x128_f8f6f4 v[110:113], v[70:77], v[62:69], v[178:181], v172, v172 op_sel_hi:[0,0,0]
	s_setprio 0
	s_barrier
	ds_read_b128 v[46:49], v171 offset:49152
	ds_read_b128 v[50:53], v171 offset:50176
	ds_read_b128 v[102:105], v171 offset:51200
	ds_read_b128 v[106:109], v171 offset:52224
	ds_read_b128 v[134:137], v171 offset:53248
	ds_read_b128 v[138:141], v171 offset:54272
	ds_read_b128 v[174:177], v171 offset:55296
	ds_read_b128 v[178:181], v171 offset:56320
	s_add_u32 s44, s42, 0x80
	s_addc_u32 s45, s43, 0
	s_mov_b32 s90, m0
	s_mov_b32 m0, s60
	s_nop 0
	global_load_lds_dwordx4 v167, s[44:45]
	s_mov_b32 m0, s90
	s_add_u32 s42, s42, 0x40080
	s_mov_b32 s90, m0
	s_mov_b32 m0, s61
	s_nop 0
	global_load_lds_dwordx4 v169, s[44:45]
	s_mov_b32 m0, s90
	s_addc_u32 s43, s43, 0
	s_mov_b32 s44, m0
	s_mov_b32 m0, s68
	s_nop 0
	global_load_lds_dwordx4 v167, s[42:43]
	s_mov_b32 m0, s44
	s_nop 0
	s_mov_b32 s44, m0
	s_mov_b32 m0, s69
	s_nop 0
	global_load_lds_dwordx4 v169, s[42:43]
	s_mov_b32 m0, s44
	s_mov_b32 s42, m0
	s_mov_b32 m0, s64
	s_nop 0
	global_load_lds_dwordx4 v166, s[40:41]
	s_mov_b32 m0, s42
	s_nop 0
	s_mov_b32 s42, m0
	s_mov_b32 m0, s65
	s_nop 0
	global_load_lds_dwordx4 v168, s[40:41]
	s_mov_b32 m0, s42
	s_waitcnt vmcnt(8)
	s_waitcnt lgkmcnt(0)
	s_barrier
	s_setprio 1
	s_waitcnt lgkmcnt(6)
	v_mfma_scale_f32_16x16x128_f8f6f4 v[98:101], v[4:11], v[46:53], v[98:101], v172, v172 op_sel_hi:[0,0,0]
	v_mfma_scale_f32_16x16x128_f8f6f4 v[94:97], v[22:29], v[46:53], v[94:97], v172, v172 op_sel_hi:[0,0,0]
	s_waitcnt lgkmcnt(4)
	v_mfma_scale_f32_16x16x128_f8f6f4 v[66:69], v[4:11], v[102:109], v[182:185], v172, v172 op_sel_hi:[0,0,0]
	v_mfma_scale_f32_16x16x128_f8f6f4 v[62:65], v[22:29], v[102:109], v[186:189], v172, v172 op_sel_hi:[0,0,0]
	s_waitcnt lgkmcnt(2)
	v_mfma_scale_f32_16x16x128_f8f6f4 v[34:37], v[4:11], v[134:141], v[190:193], v172, v172 op_sel_hi:[0,0,0]
	v_mfma_scale_f32_16x16x128_f8f6f4 v[30:33], v[22:29], v[134:141], v[194:197], v172, v172 op_sel_hi:[0,0,0]
	s_waitcnt lgkmcnt(0)
	v_mfma_scale_f32_16x16x128_f8f6f4 v[18:21], v[4:11], v[174:181], v[202:205], v172, v172 op_sel_hi:[0,0,0]
	v_mfma_scale_f32_16x16x128_f8f6f4 v[14:17], v[22:29], v[174:181], v[206:209], v172, v172 op_sel_hi:[0,0,0]
	s_setprio 0
	s_setprio 1
	v_mfma_scale_f32_16x16x128_f8f6f4 v[82:85], v[38:45], v[46:53], v[82:85], v172, v172 op_sel_hi:[0,0,0]
	v_mfma_scale_f32_16x16x128_f8f6f4 v[78:81], v[70:77], v[46:53], v[78:81], v172, v172 op_sel_hi:[0,0,0]
	v_mfma_scale_f32_16x16x128_f8f6f4 v[50:53], v[38:45], v[102:109], v[230:233], v172, v172 op_sel_hi:[0,0,0]
	v_mfma_scale_f32_16x16x128_f8f6f4 v[46:49], v[70:77], v[102:109], v[234:237], v172, v172 op_sel_hi:[0,0,0]
	v_mfma_scale_f32_16x16x128_f8f6f4 v[26:29], v[38:45], v[134:141], v[238:241], v172, v172 op_sel_hi:[0,0,0]
	v_mfma_scale_f32_16x16x128_f8f6f4 v[22:25], v[70:77], v[134:141], v[242:245], v172, v172 op_sel_hi:[0,0,0]
	v_mfma_scale_f32_16x16x128_f8f6f4 v[10:13], v[38:45], v[174:181], v[246:249], v172, v172 op_sel_hi:[0,0,0]
	v_mfma_scale_f32_16x16x128_f8f6f4 v[6:9], v[70:77], v[174:181], v[250:253], v172, v172 op_sel_hi:[0,0,0]
	s_add_u32 s85, s85, 0x100
	s_addc_u32 s86, s86, 0
	s_add_u32 s87, s87, 0x100
	s_addc_u32 s88, s88, 0
	s_cmp_ge_i32 s89, s1
	s_mov_b32 s40, s89
	s_setprio 0
	s_barrier
	s_cbranch_scc0 .LBB0_1676

.LBB0_1811:
	ds_read_b128 v[130:133], v144
	ds_read_b128 v[134:137], v144 offset:1024
	ds_read_b128 v[150:153], v144 offset:2048
	ds_read_b128 v[154:157], v144 offset:3072
	ds_read_b128 v[158:161], v145
	ds_read_b128 v[162:165], v145 offset:1024
	ds_read_b128 v[166:169], v145 offset:2048
	ds_read_b128 v[170:173], v145 offset:3072
	s_add_i32 s79, s28, 2
	s_cmp_eq_u32 s73, s28
	s_cselect_b32 s34, s68, s74
	s_cselect_b32 s35, s27, s75
	s_cselect_b32 s30, s72, s77
	s_cselect_b32 s31, s69, s78
	s_add_u32 s28, s34, 0x80
	s_addc_u32 s29, s35, 0
	ds_read_b128 v[174:177], v146
	ds_read_b128 v[178:181], v146 offset:1024
	ds_read_b128 v[182:185], v146 offset:2048
	ds_read_b128 v[186:189], v146 offset:3072
	ds_read_b128 v[190:193], v146 offset:4096
	ds_read_b128 v[194:197], v146 offset:5120
	ds_read_b128 v[202:205], v146 offset:6144
	ds_read_b128 v[206:209], v146 offset:7168
	s_add_u32 s80, s74, 0x3ff80
	s_addc_u32 s81, s75, 0
	s_mov_b32 s82, m0
	s_mov_b32 m0, s60
	s_nop 0
	global_load_lds_dwordx4 v140, s[80:81]
	s_mov_b32 m0, s82
	s_nop 0
	s_mov_b32 s82, m0
	s_mov_b32 m0, s61
	s_nop 0
	global_load_lds_dwordx4 v142, s[80:81]
	s_mov_b32 m0, s82
	s_waitcnt vmcnt(8)
	s_waitcnt lgkmcnt(0)
	s_barrier
	s_setprio 1
	s_waitcnt lgkmcnt(6)
	v_mfma_scale_f32_16x16x128_f8f6f4 v[126:129], v[130:137], v[174:181], v[126:129], v147, v147 op_sel_hi:[0,0,0]
	v_mfma_scale_f32_16x16x128_f8f6f4 v[122:125], v[150:157], v[174:181], v[122:125], v147, v147 op_sel_hi:[0,0,0]
	s_waitcnt lgkmcnt(4)
	v_mfma_scale_f32_16x16x128_f8f6f4 v[110:113], v[130:137], v[182:189], v[110:113], v147, v147 op_sel_hi:[0,0,0]
	v_mfma_scale_f32_16x16x128_f8f6f4 v[106:109], v[150:157], v[182:189], v[106:109], v147, v147 op_sel_hi:[0,0,0]
	s_waitcnt lgkmcnt(2)
	v_mfma_scale_f32_16x16x128_f8f6f4 v[198:201], v[130:137], v[190:197], v[94:97], v147, v147 op_sel_hi:[0,0,0]
	v_mfma_scale_f32_16x16x128_f8f6f4 v[210:213], v[150:157], v[190:197], v[90:93], v147, v147 op_sel_hi:[0,0,0]
	s_waitcnt lgkmcnt(0)
	v_mfma_scale_f32_16x16x128_f8f6f4 v[214:217], v[130:137], v[202:209], v[78:81], v147, v147 op_sel_hi:[0,0,0]
	v_mfma_scale_f32_16x16x128_f8f6f4 v[218:221], v[150:157], v[202:209], v[74:77], v147, v147 op_sel_hi:[0,0,0]
	s_setprio 0
	s_setprio 1
	v_mfma_scale_f32_16x16x128_f8f6f4 v[118:121], v[158:165], v[174:181], v[118:121], v147, v147 op_sel_hi:[0,0,0]
	v_mfma_scale_f32_16x16x128_f8f6f4 v[114:117], v[166:173], v[174:181], v[114:117], v147, v147 op_sel_hi:[0,0,0]
	v_mfma_scale_f32_16x16x128_f8f6f4 v[102:105], v[158:165], v[182:189], v[102:105], v147, v147 op_sel_hi:[0,0,0]
	v_mfma_scale_f32_16x16x128_f8f6f4 v[98:101], v[166:173], v[182:189], v[98:101], v147, v147 op_sel_hi:[0,0,0]
	v_mfma_scale_f32_16x16x128_f8f6f4 v[174:177], v[158:165], v[190:197], v[86:89], v147, v147 op_sel_hi:[0,0,0]
	v_mfma_scale_f32_16x16x128_f8f6f4 v[178:181], v[166:173], v[190:197], v[82:85], v147, v147 op_sel_hi:[0,0,0]
	v_mfma_scale_f32_16x16x128_f8f6f4 v[182:185], v[158:165], v[202:209], v[70:73], v147, v147 op_sel_hi:[0,0,0]
	v_mfma_scale_f32_16x16x128_f8f6f4 v[186:189], v[166:173], v[202:209], v[66:69], v147, v147 op_sel_hi:[0,0,0]
	s_setprio 0
	s_barrier
	s_nop 4
	ds_read_b128 v[66:69], v146 offset:16384
	ds_read_b128 v[70:73], v146 offset:17408
	ds_read_b128 v[74:77], v146 offset:18432
	ds_read_b128 v[78:81], v146 offset:19456
	ds_read_b128 v[82:85], v146 offset:20480
	ds_read_b128 v[86:89], v146 offset:21504
	ds_read_b128 v[90:93], v146 offset:22528
	ds_read_b128 v[94:97], v146 offset:23552
	s_mov_b32 s80, m0
	s_mov_b32 m0, s41
	s_nop 0
	global_load_lds_dwordx4 v141, s[30:31]
	s_mov_b32 m0, s80
	s_nop 0
	s_mov_b32 s80, m0
	s_mov_b32 m0, s42
	s_nop 0
	global_load_lds_dwordx4 v143, s[30:31]
	s_mov_b32 m0, s80
	s_add_u32 s80, s30, 0x40000
	s_addc_u32 s81, s31, 0
	s_mov_b32 s82, m0
	s_mov_b32 m0, s43
	s_nop 0
	global_load_lds_dwordx4 v141, s[80:81]
	s_mov_b32 m0, s82
	s_nop 0
	s_mov_b32 s82, m0
	s_mov_b32 m0, s44
	s_nop 0
	global_load_lds_dwordx4 v143, s[80:81]
	s_mov_b32 m0, s82
	s_mov_b32 s80, m0
	s_mov_b32 m0, s40
	s_nop 0
	global_load_lds_dwordx4 v140, s[34:35]
	s_mov_b32 m0, s80
	s_nop 0
	s_mov_b32 s80, m0
	s_mov_b32 m0, s45
	s_nop 0
	global_load_lds_dwordx4 v142, s[34:35]
	s_mov_b32 m0, s80
	s_waitcnt vmcnt(8)
	s_waitcnt lgkmcnt(0)
	s_barrier
	s_setprio 1
	s_waitcnt lgkmcnt(6)
	v_mfma_scale_f32_16x16x128_f8f6f4 v[62:65], v[130:137], v[66:73], v[62:65], v147, v147 op_sel_hi:[0,0,0]
	v_mfma_scale_f32_16x16x128_f8f6f4 v[58:61], v[150:157], v[66:73], v[58:61], v147, v147 op_sel_hi:[0,0,0]
	s_waitcnt lgkmcnt(4)
	v_mfma_scale_f32_16x16x128_f8f6f4 v[190:193], v[130:137], v[74:81], v[46:49], v147, v147 op_sel_hi:[0,0,0]
	v_mfma_scale_f32_16x16x128_f8f6f4 v[194:197], v[150:157], v[74:81], v[42:45], v147, v147 op_sel_hi:[0,0,0]
	s_waitcnt lgkmcnt(2)
	v_mfma_scale_f32_16x16x128_f8f6f4 v[202:205], v[130:137], v[82:89], v[30:33], v147, v147 op_sel_hi:[0,0,0]
	v_mfma_scale_f32_16x16x128_f8f6f4 v[206:209], v[150:157], v[82:89], v[26:29], v147, v147 op_sel_hi:[0,0,0]
	s_waitcnt lgkmcnt(0)
	v_mfma_scale_f32_16x16x128_f8f6f4 v[222:225], v[130:137], v[90:97], v[14:17], v147, v147 op_sel_hi:[0,0,0]
	v_mfma_scale_f32_16x16x128_f8f6f4 v[226:229], v[150:157], v[90:97], v[10:13], v147, v147 op_sel_hi:[0,0,0]
	s_setprio 0
	s_setprio 1
	v_mfma_scale_f32_16x16x128_f8f6f4 v[54:57], v[158:165], v[66:73], v[54:57], v147, v147 op_sel_hi:[0,0,0]
	v_mfma_scale_f32_16x16x128_f8f6f4 v[50:53], v[166:173], v[66:73], v[50:53], v147, v147 op_sel_hi:[0,0,0]
	v_mfma_scale_f32_16x16x128_f8f6f4 v[230:233], v[158:165], v[74:81], v[38:41], v147, v147 op_sel_hi:[0,0,0]
	v_mfma_scale_f32_16x16x128_f8f6f4 v[234:237], v[166:173], v[74:81], v[34:37], v147, v147 op_sel_hi:[0,0,0]
	v_mfma_scale_f32_16x16x128_f8f6f4 v[238:241], v[158:165], v[82:89], v[22:25], v147, v147 op_sel_hi:[0,0,0]
	v_mfma_scale_f32_16x16x128_f8f6f4 v[242:245], v[166:173], v[82:89], v[18:21], v147, v147 op_sel_hi:[0,0,0]
	v_mfma_scale_f32_16x16x128_f8f6f4 v[246:249], v[158:165], v[90:97], v[6:9], v147, v147 op_sel_hi:[0,0,0]
	v_mfma_scale_f32_16x16x128_f8f6f4 v[250:253], v[166:173], v[90:97], v[2:5], v147, v147 op_sel_hi:[0,0,0]
	s_setprio 0
	s_barrier
	s_nop 4
	ds_read_b128 v[2:5], v148
	ds_read_b128 v[6:9], v148 offset:1024
	ds_read_b128 v[18:21], v148 offset:2048
	ds_read_b128 v[22:25], v148 offset:3072
	ds_read_b128 v[130:133], v149
	ds_read_b128 v[134:137], v149 offset:1024
	ds_read_b128 v[150:153], v149 offset:2048
	ds_read_b128 v[154:157], v149 offset:3072
	ds_read_b128 v[10:13], v146 offset:32768
	ds_read_b128 v[14:17], v146 offset:33792
	ds_read_b128 v[26:29], v146 offset:34816
	ds_read_b128 v[30:33], v146 offset:35840
	ds_read_b128 v[34:37], v146 offset:36864
	ds_read_b128 v[38:41], v146 offset:37888
	ds_read_b128 v[42:45], v146 offset:38912
	ds_read_b128 v[46:49], v146 offset:39936
	s_add_u32 s34, s34, 0x40000
	s_addc_u32 s35, s35, 0
	s_mov_b32 s80, m0
	s_mov_b32 m0, s46
	s_nop 0
	global_load_lds_dwordx4 v140, s[34:35]
	s_mov_b32 m0, s80
	s_nop 0
	s_mov_b32 s80, m0
	s_mov_b32 m0, s47
	s_nop 0
	global_load_lds_dwordx4 v142, s[34:35]
	s_mov_b32 m0, s80
	s_waitcnt vmcnt(8)
	s_waitcnt lgkmcnt(0)
	s_barrier
	s_setprio 1
	s_waitcnt lgkmcnt(6)
	v_mfma_scale_f32_16x16x128_f8f6f4 v[126:129], v[2:9], v[10:17], v[126:129], v147, v147 op_sel_hi:[0,0,0]
	v_mfma_scale_f32_16x16x128_f8f6f4 v[122:125], v[18:25], v[10:17], v[122:125], v147, v147 op_sel_hi:[0,0,0]
	s_waitcnt lgkmcnt(4)
	v_mfma_scale_f32_16x16x128_f8f6f4 v[110:113], v[2:9], v[26:33], v[110:113], v147, v147 op_sel_hi:[0,0,0]
	v_mfma_scale_f32_16x16x128_f8f6f4 v[106:109], v[18:25], v[26:33], v[106:109], v147, v147 op_sel_hi:[0,0,0]
	s_waitcnt lgkmcnt(2)
	v_mfma_scale_f32_16x16x128_f8f6f4 v[94:97], v[2:9], v[34:41], v[198:201], v147, v147 op_sel_hi:[0,0,0]
	v_mfma_scale_f32_16x16x128_f8f6f4 v[90:93], v[18:25], v[34:41], v[210:213], v147, v147 op_sel_hi:[0,0,0]
	s_waitcnt lgkmcnt(0)
	v_mfma_scale_f32_16x16x128_f8f6f4 v[78:81], v[2:9], v[42:49], v[214:217], v147, v147 op_sel_hi:[0,0,0]
	v_mfma_scale_f32_16x16x128_f8f6f4 v[74:77], v[18:25], v[42:49], v[218:221], v147, v147 op_sel_hi:[0,0,0]
	s_setprio 0
	s_setprio 1
	v_mfma_scale_f32_16x16x128_f8f6f4 v[118:121], v[130:137], v[10:17], v[118:121], v147, v147 op_sel_hi:[0,0,0]
	v_mfma_scale_f32_16x16x128_f8f6f4 v[114:117], v[150:157], v[10:17], v[114:117], v147, v147 op_sel_hi:[0,0,0]
	v_mfma_scale_f32_16x16x128_f8f6f4 v[102:105], v[130:137], v[26:33], v[102:105], v147, v147 op_sel_hi:[0,0,0]
	v_mfma_scale_f32_16x16x128_f8f6f4 v[98:101], v[150:157], v[26:33], v[98:101], v147, v147 op_sel_hi:[0,0,0]
	v_mfma_scale_f32_16x16x128_f8f6f4 v[86:89], v[130:137], v[34:41], v[174:177], v147, v147 op_sel_hi:[0,0,0]
	v_mfma_scale_f32_16x16x128_f8f6f4 v[82:85], v[150:157], v[34:41], v[178:181], v147, v147 op_sel_hi:[0,0,0]
	v_mfma_scale_f32_16x16x128_f8f6f4 v[70:73], v[130:137], v[42:49], v[182:185], v147, v147 op_sel_hi:[0,0,0]
	v_mfma_scale_f32_16x16x128_f8f6f4 v[66:69], v[150:157], v[42:49], v[186:189], v147, v147 op_sel_hi:[0,0,0]
	s_setprio 0
	s_barrier
	ds_read_b128 v[34:37], v146 offset:49152
	ds_read_b128 v[38:41], v146 offset:50176
	ds_read_b128 v[158:161], v146 offset:51200
	ds_read_b128 v[162:165], v146 offset:52224
	ds_read_b128 v[166:169], v146 offset:53248
	ds_read_b128 v[170:173], v146 offset:54272
	ds_read_b128 v[174:177], v146 offset:55296
	ds_read_b128 v[178:181], v146 offset:56320
	s_add_u32 s34, s30, 0x80
	s_addc_u32 s35, s31, 0
	s_mov_b32 s80, m0
	s_mov_b32 m0, s54
	s_nop 0
	global_load_lds_dwordx4 v141, s[34:35]
	s_mov_b32 m0, s80
	s_add_u32 s30, s30, 0x40080
	s_mov_b32 s80, m0
	s_mov_b32 m0, s55
	s_nop 0
	global_load_lds_dwordx4 v143, s[34:35]
	s_mov_b32 m0, s80
	s_addc_u32 s31, s31, 0
	s_mov_b32 s34, m0
	s_mov_b32 m0, s58
	s_nop 0
	global_load_lds_dwordx4 v141, s[30:31]
	s_mov_b32 m0, s34
	s_nop 0
	s_mov_b32 s34, m0
	s_mov_b32 m0, s59
	s_nop 0
	global_load_lds_dwordx4 v143, s[30:31]
	s_mov_b32 m0, s34
	s_mov_b32 s30, m0
	s_mov_b32 m0, s56
	s_nop 0
	global_load_lds_dwordx4 v140, s[28:29]
	s_mov_b32 m0, s30
	s_nop 0
	s_mov_b32 s30, m0
	s_mov_b32 m0, s57
	s_nop 0
	global_load_lds_dwordx4 v142, s[28:29]
	s_mov_b32 m0, s30
	s_waitcnt vmcnt(8)
	s_waitcnt lgkmcnt(0)
	s_barrier
	s_setprio 1
	s_waitcnt lgkmcnt(6)
	v_mfma_scale_f32_16x16x128_f8f6f4 v[62:65], v[2:9], v[34:41], v[62:65], v147, v147 op_sel_hi:[0,0,0]
	v_mfma_scale_f32_16x16x128_f8f6f4 v[58:61], v[18:25], v[34:41], v[58:61], v147, v147 op_sel_hi:[0,0,0]
	s_waitcnt lgkmcnt(4)
	v_mfma_scale_f32_16x16x128_f8f6f4 v[46:49], v[2:9], v[158:165], v[190:193], v147, v147 op_sel_hi:[0,0,0]
	v_mfma_scale_f32_16x16x128_f8f6f4 v[42:45], v[18:25], v[158:165], v[194:197], v147, v147 op_sel_hi:[0,0,0]
	s_waitcnt lgkmcnt(2)
	v_mfma_scale_f32_16x16x128_f8f6f4 v[30:33], v[2:9], v[166:173], v[202:205], v147, v147 op_sel_hi:[0,0,0]
	v_mfma_scale_f32_16x16x128_f8f6f4 v[26:29], v[18:25], v[166:173], v[206:209], v147, v147 op_sel_hi:[0,0,0]
	s_waitcnt lgkmcnt(0)
	v_mfma_scale_f32_16x16x128_f8f6f4 v[14:17], v[2:9], v[174:181], v[222:225], v147, v147 op_sel_hi:[0,0,0]
	v_mfma_scale_f32_16x16x128_f8f6f4 v[10:13], v[18:25], v[174:181], v[226:229], v147, v147 op_sel_hi:[0,0,0]
	s_setprio 0
	s_setprio 1
	v_mfma_scale_f32_16x16x128_f8f6f4 v[54:57], v[130:137], v[34:41], v[54:57], v147, v147 op_sel_hi:[0,0,0]
	v_mfma_scale_f32_16x16x128_f8f6f4 v[50:53], v[150:157], v[34:41], v[50:53], v147, v147 op_sel_hi:[0,0,0]
	v_mfma_scale_f32_16x16x128_f8f6f4 v[38:41], v[130:137], v[158:165], v[230:233], v147, v147 op_sel_hi:[0,0,0]
	v_mfma_scale_f32_16x16x128_f8f6f4 v[34:37], v[150:157], v[158:165], v[234:237], v147, v147 op_sel_hi:[0,0,0]
	v_mfma_scale_f32_16x16x128_f8f6f4 v[22:25], v[130:137], v[166:173], v[238:241], v147, v147 op_sel_hi:[0,0,0]
	v_mfma_scale_f32_16x16x128_f8f6f4 v[18:21], v[150:157], v[166:173], v[242:245], v147, v147 op_sel_hi:[0,0,0]
	v_mfma_scale_f32_16x16x128_f8f6f4 v[6:9], v[130:137], v[174:181], v[246:249], v147, v147 op_sel_hi:[0,0,0]
	v_mfma_scale_f32_16x16x128_f8f6f4 v[2:5], v[150:157], v[174:181], v[250:253], v147, v147 op_sel_hi:[0,0,0]
	s_add_u32 s74, s74, 0x100
	s_addc_u32 s75, s75, 0
	s_add_u32 s77, s77, 0x100
	s_addc_u32 s78, s78, 0
	s_cmp_ge_i32 s79, s19
	s_mov_b32 s28, s79
	s_setprio 0
	s_barrier
	s_cbranch_scc0 .LBB0_1811
	s_and_b64 vcc, exec, s[8:9]
	s_cbranch_vccz .LBB0_1814

.LBB0_2095:
	ds_read_b128 v[140:143], v1
	ds_read_b128 v[144:147], v1 offset:1024
	ds_read_b128 v[148:151], v1 offset:2048
	ds_read_b128 v[152:155], v1 offset:3072
	ds_read_b128 v[156:159], v134
	ds_read_b128 v[160:163], v134 offset:1024
	ds_read_b128 v[164:167], v134 offset:2048
	ds_read_b128 v[168:171], v134 offset:3072
	s_add_i32 s65, s14, 2
	s_cmp_eq_u32 s60, s14
	s_cselect_b32 s18, s57, s61
	s_cselect_b32 s19, s56, s62
	s_cselect_b32 s16, s59, s63
	s_cselect_b32 s17, s58, s64
	s_add_u32 s14, s18, 0x80
	s_addc_u32 s15, s19, 0
	ds_read_b128 v[172:175], v135
	ds_read_b128 v[176:179], v135 offset:1024
	ds_read_b128 v[180:183], v135 offset:2048
	ds_read_b128 v[184:187], v135 offset:3072
	ds_read_b128 v[188:191], v135 offset:4096
	ds_read_b128 v[192:195], v135 offset:5120
	ds_read_b128 v[202:205], v135 offset:6144
	ds_read_b128 v[206:209], v135 offset:7168
	s_add_u32 s66, s61, 0xff80
	s_addc_u32 s67, s62, 0
	s_mov_b32 s68, m0
	s_mov_b32 m0, s40
	s_nop 0
	global_load_lds_dwordx4 v130, s[66:67]
	s_mov_b32 m0, s68
	s_nop 0
	s_mov_b32 s68, m0
	s_mov_b32 m0, s41
	s_nop 0
	global_load_lds_dwordx4 v132, s[66:67]
	s_mov_b32 m0, s68
	s_waitcnt vmcnt(8)
	s_waitcnt lgkmcnt(0)
	s_barrier
	s_setprio 1
	s_waitcnt lgkmcnt(6)
	v_mfma_scale_f32_16x16x128_f8f6f4 v[126:129], v[140:147], v[172:179], v[126:129], v136, v136 op_sel_hi:[0,0,0]
	v_mfma_scale_f32_16x16x128_f8f6f4 v[122:125], v[148:155], v[172:179], v[122:125], v136, v136 op_sel_hi:[0,0,0]
	s_waitcnt lgkmcnt(4)
	v_mfma_scale_f32_16x16x128_f8f6f4 v[110:113], v[140:147], v[180:187], v[110:113], v136, v136 op_sel_hi:[0,0,0]
	v_mfma_scale_f32_16x16x128_f8f6f4 v[106:109], v[148:155], v[180:187], v[106:109], v136, v136 op_sel_hi:[0,0,0]
	s_waitcnt lgkmcnt(2)
	v_mfma_scale_f32_16x16x128_f8f6f4 v[196:199], v[140:147], v[188:195], v[94:97], v136, v136 op_sel_hi:[0,0,0]
	v_mfma_scale_f32_16x16x128_f8f6f4 v[210:213], v[148:155], v[188:195], v[90:93], v136, v136 op_sel_hi:[0,0,0]
	s_waitcnt lgkmcnt(0)
	v_mfma_scale_f32_16x16x128_f8f6f4 v[214:217], v[140:147], v[202:209], v[78:81], v136, v136 op_sel_hi:[0,0,0]
	v_mfma_scale_f32_16x16x128_f8f6f4 v[218:221], v[148:155], v[202:209], v[74:77], v136, v136 op_sel_hi:[0,0,0]
	s_setprio 0
	s_setprio 1
	v_mfma_scale_f32_16x16x128_f8f6f4 v[118:121], v[156:163], v[172:179], v[118:121], v136, v136 op_sel_hi:[0,0,0]
	v_mfma_scale_f32_16x16x128_f8f6f4 v[114:117], v[164:171], v[172:179], v[114:117], v136, v136 op_sel_hi:[0,0,0]
	v_mfma_scale_f32_16x16x128_f8f6f4 v[102:105], v[156:163], v[180:187], v[102:105], v136, v136 op_sel_hi:[0,0,0]
	v_mfma_scale_f32_16x16x128_f8f6f4 v[98:101], v[164:171], v[180:187], v[98:101], v136, v136 op_sel_hi:[0,0,0]
	v_mfma_scale_f32_16x16x128_f8f6f4 v[172:175], v[156:163], v[188:195], v[86:89], v136, v136 op_sel_hi:[0,0,0]
	v_mfma_scale_f32_16x16x128_f8f6f4 v[176:179], v[164:171], v[188:195], v[82:85], v136, v136 op_sel_hi:[0,0,0]
	v_mfma_scale_f32_16x16x128_f8f6f4 v[180:183], v[156:163], v[202:209], v[70:73], v136, v136 op_sel_hi:[0,0,0]
	v_mfma_scale_f32_16x16x128_f8f6f4 v[184:187], v[164:171], v[202:209], v[66:69], v136, v136 op_sel_hi:[0,0,0]
	s_setprio 0
	s_barrier
	s_nop 4
	ds_read_b128 v[66:69], v135 offset:16384
	ds_read_b128 v[70:73], v135 offset:17408
	ds_read_b128 v[74:77], v135 offset:18432
	ds_read_b128 v[78:81], v135 offset:19456
	ds_read_b128 v[82:85], v135 offset:20480
	ds_read_b128 v[86:89], v135 offset:21504
	ds_read_b128 v[90:93], v135 offset:22528
	ds_read_b128 v[94:97], v135 offset:23552
	s_mov_b32 s66, m0
	s_mov_b32 m0, s23
	s_nop 0
	global_load_lds_dwordx4 v131, s[16:17]
	s_mov_b32 m0, s66
	s_nop 0
	s_mov_b32 s66, m0
	s_mov_b32 m0, s24
	s_nop 0
	global_load_lds_dwordx4 v133, s[16:17]
	s_mov_b32 m0, s66
	s_add_u32 s66, s16, 0x10000
	s_addc_u32 s67, s17, 0
	s_mov_b32 s68, m0
	s_mov_b32 m0, s25
	s_nop 0
	global_load_lds_dwordx4 v131, s[66:67]
	s_mov_b32 m0, s68
	s_nop 0
	s_mov_b32 s68, m0
	s_mov_b32 m0, s26
	s_nop 0
	global_load_lds_dwordx4 v133, s[66:67]
	s_mov_b32 m0, s68
	s_mov_b32 s66, m0
	s_mov_b32 m0, s22
	s_nop 0
	global_load_lds_dwordx4 v130, s[18:19]
	s_mov_b32 m0, s66
	s_nop 0
	s_mov_b32 s66, m0
	s_mov_b32 m0, s27
	s_nop 0
	global_load_lds_dwordx4 v132, s[18:19]
	s_mov_b32 m0, s66
	s_waitcnt vmcnt(8)
	s_waitcnt lgkmcnt(0)
	s_barrier
	s_setprio 1
	s_waitcnt lgkmcnt(6)
	v_mfma_scale_f32_16x16x128_f8f6f4 v[62:65], v[140:147], v[66:73], v[62:65], v136, v136 op_sel_hi:[0,0,0]
	v_mfma_scale_f32_16x16x128_f8f6f4 v[58:61], v[148:155], v[66:73], v[58:61], v136, v136 op_sel_hi:[0,0,0]
	s_waitcnt lgkmcnt(4)
	v_mfma_scale_f32_16x16x128_f8f6f4 v[188:191], v[140:147], v[74:81], v[46:49], v136, v136 op_sel_hi:[0,0,0]
	v_mfma_scale_f32_16x16x128_f8f6f4 v[192:195], v[148:155], v[74:81], v[42:45], v136, v136 op_sel_hi:[0,0,0]
	s_waitcnt lgkmcnt(2)
	v_mfma_scale_f32_16x16x128_f8f6f4 v[200:203], v[140:147], v[82:89], v[30:33], v136, v136 op_sel_hi:[0,0,0]
	v_mfma_scale_f32_16x16x128_f8f6f4 v[204:207], v[148:155], v[82:89], v[26:29], v136, v136 op_sel_hi:[0,0,0]
	s_waitcnt lgkmcnt(0)
	v_mfma_scale_f32_16x16x128_f8f6f4 v[222:225], v[140:147], v[90:97], v[14:17], v136, v136 op_sel_hi:[0,0,0]
	v_mfma_scale_f32_16x16x128_f8f6f4 v[226:229], v[148:155], v[90:97], v[10:13], v136, v136 op_sel_hi:[0,0,0]
	s_setprio 0
	s_setprio 1
	v_mfma_scale_f32_16x16x128_f8f6f4 v[54:57], v[156:163], v[66:73], v[54:57], v136, v136 op_sel_hi:[0,0,0]
	v_mfma_scale_f32_16x16x128_f8f6f4 v[50:53], v[164:171], v[66:73], v[50:53], v136, v136 op_sel_hi:[0,0,0]
	v_mfma_scale_f32_16x16x128_f8f6f4 v[230:233], v[156:163], v[74:81], v[38:41], v136, v136 op_sel_hi:[0,0,0]
	v_mfma_scale_f32_16x16x128_f8f6f4 v[234:237], v[164:171], v[74:81], v[34:37], v136, v136 op_sel_hi:[0,0,0]
	v_mfma_scale_f32_16x16x128_f8f6f4 v[238:241], v[156:163], v[82:89], v[22:25], v136, v136 op_sel_hi:[0,0,0]
	v_mfma_scale_f32_16x16x128_f8f6f4 v[242:245], v[164:171], v[82:89], v[18:21], v136, v136 op_sel_hi:[0,0,0]
	v_mfma_scale_f32_16x16x128_f8f6f4 v[246:249], v[156:163], v[90:97], v[6:9], v136, v136 op_sel_hi:[0,0,0]
	v_mfma_scale_f32_16x16x128_f8f6f4 v[250:253], v[164:171], v[90:97], v[2:5], v136, v136 op_sel_hi:[0,0,0]
	s_setprio 0
	s_barrier
	s_nop 4
	ds_read_b128 v[2:5], v137
	ds_read_b128 v[6:9], v137 offset:1024
	ds_read_b128 v[18:21], v137 offset:2048
	ds_read_b128 v[22:25], v137 offset:3072
	ds_read_b128 v[140:143], v138
	ds_read_b128 v[144:147], v138 offset:1024
	ds_read_b128 v[148:151], v138 offset:2048
	ds_read_b128 v[152:155], v138 offset:3072
	ds_read_b128 v[10:13], v135 offset:32768
	ds_read_b128 v[14:17], v135 offset:33792
	ds_read_b128 v[26:29], v135 offset:34816
	ds_read_b128 v[30:33], v135 offset:35840
	ds_read_b128 v[34:37], v135 offset:36864
	ds_read_b128 v[38:41], v135 offset:37888
	ds_read_b128 v[42:45], v135 offset:38912
	ds_read_b128 v[46:49], v135 offset:39936
	s_add_u32 s18, s18, 0x10000
	s_addc_u32 s19, s19, 0
	s_mov_b32 s66, m0
	s_mov_b32 m0, s28
	s_nop 0
	global_load_lds_dwordx4 v130, s[18:19]
	s_mov_b32 m0, s66
	s_nop 0
	s_mov_b32 s66, m0
	s_mov_b32 m0, s29
	s_nop 0
	global_load_lds_dwordx4 v132, s[18:19]
	s_mov_b32 m0, s66
	s_waitcnt vmcnt(8)
	s_waitcnt lgkmcnt(0)
	s_barrier
	s_setprio 1
	s_waitcnt lgkmcnt(6)
	v_mfma_scale_f32_16x16x128_f8f6f4 v[126:129], v[2:9], v[10:17], v[126:129], v136, v136 op_sel_hi:[0,0,0]
	v_mfma_scale_f32_16x16x128_f8f6f4 v[122:125], v[18:25], v[10:17], v[122:125], v136, v136 op_sel_hi:[0,0,0]
	s_waitcnt lgkmcnt(4)
	v_mfma_scale_f32_16x16x128_f8f6f4 v[110:113], v[2:9], v[26:33], v[110:113], v136, v136 op_sel_hi:[0,0,0]
	v_mfma_scale_f32_16x16x128_f8f6f4 v[106:109], v[18:25], v[26:33], v[106:109], v136, v136 op_sel_hi:[0,0,0]
	s_waitcnt lgkmcnt(2)
	v_mfma_scale_f32_16x16x128_f8f6f4 v[94:97], v[2:9], v[34:41], v[196:199], v136, v136 op_sel_hi:[0,0,0]
	v_mfma_scale_f32_16x16x128_f8f6f4 v[90:93], v[18:25], v[34:41], v[210:213], v136, v136 op_sel_hi:[0,0,0]
	s_waitcnt lgkmcnt(0)
	v_mfma_scale_f32_16x16x128_f8f6f4 v[78:81], v[2:9], v[42:49], v[214:217], v136, v136 op_sel_hi:[0,0,0]
	v_mfma_scale_f32_16x16x128_f8f6f4 v[74:77], v[18:25], v[42:49], v[218:221], v136, v136 op_sel_hi:[0,0,0]
	s_setprio 0
	s_setprio 1
	v_mfma_scale_f32_16x16x128_f8f6f4 v[118:121], v[140:147], v[10:17], v[118:121], v136, v136 op_sel_hi:[0,0,0]
	v_mfma_scale_f32_16x16x128_f8f6f4 v[114:117], v[148:155], v[10:17], v[114:117], v136, v136 op_sel_hi:[0,0,0]
	v_mfma_scale_f32_16x16x128_f8f6f4 v[102:105], v[140:147], v[26:33], v[102:105], v136, v136 op_sel_hi:[0,0,0]
	v_mfma_scale_f32_16x16x128_f8f6f4 v[98:101], v[148:155], v[26:33], v[98:101], v136, v136 op_sel_hi:[0,0,0]
	v_mfma_scale_f32_16x16x128_f8f6f4 v[86:89], v[140:147], v[34:41], v[172:175], v136, v136 op_sel_hi:[0,0,0]
	v_mfma_scale_f32_16x16x128_f8f6f4 v[82:85], v[148:155], v[34:41], v[176:179], v136, v136 op_sel_hi:[0,0,0]
	v_mfma_scale_f32_16x16x128_f8f6f4 v[70:73], v[140:147], v[42:49], v[180:183], v136, v136 op_sel_hi:[0,0,0]
	v_mfma_scale_f32_16x16x128_f8f6f4 v[66:69], v[148:155], v[42:49], v[184:187], v136, v136 op_sel_hi:[0,0,0]
	s_setprio 0
	s_barrier
	ds_read_b128 v[34:37], v135 offset:49152
	ds_read_b128 v[38:41], v135 offset:50176
	ds_read_b128 v[156:159], v135 offset:51200
	ds_read_b128 v[160:163], v135 offset:52224
	ds_read_b128 v[164:167], v135 offset:53248
	ds_read_b128 v[168:171], v135 offset:54272
	ds_read_b128 v[172:175], v135 offset:55296
	ds_read_b128 v[176:179], v135 offset:56320
	s_add_u32 s18, s16, 0x80
	s_addc_u32 s19, s17, 0
	s_mov_b32 s66, m0
	s_mov_b32 m0, s34
	s_nop 0
	global_load_lds_dwordx4 v131, s[18:19]
	s_mov_b32 m0, s66
	s_add_u32 s16, s16, 0x10080
	s_mov_b32 s66, m0
	s_mov_b32 m0, s35
	s_nop 0
	global_load_lds_dwordx4 v133, s[18:19]
	s_mov_b32 m0, s66
	s_addc_u32 s17, s17, 0
	s_mov_b32 s18, m0
	s_mov_b32 m0, s38
	s_nop 0
	global_load_lds_dwordx4 v131, s[16:17]
	s_mov_b32 m0, s18
	s_nop 0
	s_mov_b32 s18, m0
	s_mov_b32 m0, s39
	s_nop 0
	global_load_lds_dwordx4 v133, s[16:17]
	s_mov_b32 m0, s18
	s_mov_b32 s16, m0
	s_mov_b32 m0, s36
	s_nop 0
	global_load_lds_dwordx4 v130, s[14:15]
	s_mov_b32 m0, s16
	s_nop 0
	s_mov_b32 s16, m0
	s_mov_b32 m0, s37
	s_nop 0
	global_load_lds_dwordx4 v132, s[14:15]
	s_mov_b32 m0, s16
	s_waitcnt vmcnt(8)
	s_waitcnt lgkmcnt(0)
	s_barrier
	s_setprio 1
	s_waitcnt lgkmcnt(6)
	v_mfma_scale_f32_16x16x128_f8f6f4 v[62:65], v[2:9], v[34:41], v[62:65], v136, v136 op_sel_hi:[0,0,0]
	v_mfma_scale_f32_16x16x128_f8f6f4 v[58:61], v[18:25], v[34:41], v[58:61], v136, v136 op_sel_hi:[0,0,0]
	s_waitcnt lgkmcnt(4)
	v_mfma_scale_f32_16x16x128_f8f6f4 v[46:49], v[2:9], v[156:163], v[188:191], v136, v136 op_sel_hi:[0,0,0]
	v_mfma_scale_f32_16x16x128_f8f6f4 v[42:45], v[18:25], v[156:163], v[192:195], v136, v136 op_sel_hi:[0,0,0]
	s_waitcnt lgkmcnt(2)
	v_mfma_scale_f32_16x16x128_f8f6f4 v[30:33], v[2:9], v[164:171], v[200:203], v136, v136 op_sel_hi:[0,0,0]
	v_mfma_scale_f32_16x16x128_f8f6f4 v[26:29], v[18:25], v[164:171], v[204:207], v136, v136 op_sel_hi:[0,0,0]
	s_waitcnt lgkmcnt(0)
	v_mfma_scale_f32_16x16x128_f8f6f4 v[14:17], v[2:9], v[172:179], v[222:225], v136, v136 op_sel_hi:[0,0,0]
	v_mfma_scale_f32_16x16x128_f8f6f4 v[10:13], v[18:25], v[172:179], v[226:229], v136, v136 op_sel_hi:[0,0,0]
	s_setprio 0
	s_setprio 1
	v_mfma_scale_f32_16x16x128_f8f6f4 v[54:57], v[140:147], v[34:41], v[54:57], v136, v136 op_sel_hi:[0,0,0]
	v_mfma_scale_f32_16x16x128_f8f6f4 v[50:53], v[148:155], v[34:41], v[50:53], v136, v136 op_sel_hi:[0,0,0]
	v_mfma_scale_f32_16x16x128_f8f6f4 v[38:41], v[140:147], v[156:163], v[230:233], v136, v136 op_sel_hi:[0,0,0]
	v_mfma_scale_f32_16x16x128_f8f6f4 v[34:37], v[148:155], v[156:163], v[234:237], v136, v136 op_sel_hi:[0,0,0]
	v_mfma_scale_f32_16x16x128_f8f6f4 v[22:25], v[140:147], v[164:171], v[238:241], v136, v136 op_sel_hi:[0,0,0]
	v_mfma_scale_f32_16x16x128_f8f6f4 v[18:21], v[148:155], v[164:171], v[242:245], v136, v136 op_sel_hi:[0,0,0]
	v_mfma_scale_f32_16x16x128_f8f6f4 v[6:9], v[140:147], v[172:179], v[246:249], v136, v136 op_sel_hi:[0,0,0]
	v_mfma_scale_f32_16x16x128_f8f6f4 v[2:5], v[148:155], v[172:179], v[250:253], v136, v136 op_sel_hi:[0,0,0]
	s_add_u32 s61, s61, 0x100
	s_addc_u32 s62, s62, 0
	s_add_u32 s63, s63, 0x100
	s_addc_u32 s64, s64, 0
	s_cmp_ge_i32 s65, s55
	s_mov_b32 s14, s65
	s_setprio 0
	s_barrier
	s_cbranch_scc0 .LBB0_2095
	s_and_b64 vcc, exec, s[4:5]
	s_cbranch_vccz .LBB0_2098
